# v14 + P8 prologue de-serialisation: first row's four x2 loads issued right behind the row-statistics load (ahead of the rstd chain and barrier); router bias load hoisted out of the 3-trip reduce loop
# baseline (speedup 1.0000x reference)
.LBB0_985:
	v_readfirstlane_b32 s1, v0
	s_and_saveexec_b64 s[2:3], s[8:9]
	ds_write_b32 v1, v37 offset:42496
	s_or_b64 exec, exec, s[2:3]
	s_lshl_b32 s5, s4, 6
	v_or_b32_e32 v2, s5, v35
	v_ashrrev_i32_e32 v3, 31, v2
	v_lshlrev_b64 v[2:3], 7, v[2:3]
	v_lshl_add_u64 v[2:3], v[38:39], 0, v[2:3]
	global_load_dwordx4 v[2:5], v[2:3], off
	s_andn2_b64 vcc, exec, s[90:91]
	s_lshr_b32 s12, s1, 6
	s_cbranch_vccnz .Lp8_nopf
	s_lshl_b32 s12, s12, 3
	s_add_i32 s12, s12, s5
	s_ashr_i32 s13, s12, 31
	s_lshl_b64 s[12:13], s[12:13], 12
	v_lshl_add_u64 v[180:181], v[40:41], 0, s[12:13]
	global_load_dwordx4 v[10:13], v[180:181], off
	global_load_dwordx4 v[26:29], v[180:181], off offset:1024
	global_load_dwordx4 v[30:33], v[180:181], off offset:2048
	global_load_dwordx4 v[58:61], v[180:181], off offset:3072
	s_waitcnt vmcnt(4)
	s_branch .Lp8_join

.Lp8_join:
	v_add_f32_e32 v2, v2, v3
	v_add_f32_e32 v3, v4, v5
	v_add_f32_e32 v2, v2, v3
	ds_bpermute_b32 v3, v62, v2
	s_waitcnt lgkmcnt(0)
	v_add_f32_e32 v2, v2, v3
	ds_bpermute_b32 v3, v63, v2
	s_waitcnt lgkmcnt(0)
	v_add_f32_e32 v2, v2, v3
	ds_bpermute_b32 v3, v64, v2
	s_and_saveexec_b64 s[2:3], s[10:11]
	s_cbranch_execz .LBB0_989
	s_waitcnt lgkmcnt(0)
	v_add_f32_e32 v2, v2, v3
	v_fmamk_f32 v2, v2, 0x3a000000, v71
	s_mov_b32 s0, 0xf800000
	v_mul_f32_e32 v3, 0x4f800000, v2
	v_cmp_gt_f32_e32 vcc, s0, v2
	s_nop 1
	v_cndmask_b32_e32 v2, v2, v3, vcc
	v_sqrt_f32_e32 v3, v2
	s_nop 0
	v_add_u32_e32 v4, -1, v3
	v_fma_f32 v6, -v4, v3, v2
	v_add_u32_e32 v5, 1, v3
	v_cmp_ge_f32_e64 s[12:13], 0, v6
	s_nop 1
	v_cndmask_b32_e64 v4, v3, v4, s[12:13]
	v_fma_f32 v3, -v5, v3, v2
	v_cmp_lt_f32_e64 s[12:13], 0, v3
	s_nop 1
	v_cndmask_b32_e64 v3, v4, v5, s[12:13]
	v_mul_f32_e32 v4, 0x37800000, v3
	v_cndmask_b32_e32 v3, v3, v4, vcc
	v_cmp_class_f32_e32 vcc, v2, v72
	s_nop 1
	v_cndmask_b32_e32 v2, v3, v2, vcc
	v_div_scale_f32 v3, s[12:13], v2, v2, 1.0
	v_rcp_f32_e32 v4, v3
	s_nop 0
	v_fma_f32 v5, -v3, v4, 1.0
	v_fmac_f32_e32 v4, v5, v4
	v_div_scale_f32 v5, vcc, 1.0, v2, 1.0
	v_mul_f32_e32 v6, v5, v4
	v_fma_f32 v7, -v3, v6, v5
	v_fmac_f32_e32 v6, v7, v4
	v_fma_f32 v3, -v3, v6, v5
	v_div_fmas_f32 v3, v3, v4, v6
	v_div_fixup_f32 v2, v3, v2, 1.0
	ds_write_b32 v65, v2
.LBB0_989:
	s_or_b64 exec, exec, s[2:3]
	s_andn2_b64 vcc, exec, s[90:91]
	s_lshr_b32 s0, s1, 6
	s_cbranch_vccnz .LBB0_991
	s_lshl_b32 s2, s0, 3
	s_add_i32 s12, s2, s5
	s_ashr_i32 s13, s12, 31
	s_lshl_b64 s[2:3], s[12:13], 12
	v_lshl_add_u64 v[22:23], v[40:41], 0, s[2:3]
	s_waitcnt lgkmcnt(0)
	s_barrier
	s_waitcnt vmcnt(0)
	v_mov_b64_e32 v[18:19], v[120:121]
	v_mov_b64_e32 v[20:21], v[122:123]
	v_mov_b64_e32 v[14:15], v[124:125]
	v_mov_b64_e32 v[16:17], v[126:127]
	s_lshl_b32 s2, s0, 5
	s_add_i32 s2, s2, 0
	v_mov_b32_e32 v2, s2
	ds_read_b128 v[6:9], v2
	ds_read_b128 v[2:5], v2 offset:16
	v_mov_b32_e32 v24, v37
	v_mov_b32_e32 v25, v37
	s_add_i32 s14, s12, 1
	s_ashr_i32 s15, s14, 31
	s_lshl_b64 s[16:17], s[12:13], 11
	s_lshl_b64 s[2:3], s[14:15], 12
	v_lshl_add_u64 v[86:87], v[44:45], 0, s[16:17]
	v_lshl_add_u64 v[22:23], v[40:41], 0, s[2:3]
	v_mov_b32_e32 v88, v37
	v_mov_b32_e32 v89, v37
	s_add_i32 s2, s12, 2
	s_ashr_i32 s3, s2, 31
	s_lshl_b64 s[16:17], s[2:3], 12
	s_lshl_b64 s[14:15], s[14:15], 11
	s_lshl_b64 s[2:3], s[2:3], 11
	s_waitcnt vmcnt(3)
	v_lshlrev_b32_e32 v36, 16, v10
	v_and_b32_e32 v10, 0xffff0000, v10
	v_lshlrev_b32_e32 v78, 16, v12
	v_and_b32_e32 v12, 0xffff0000, v12
	s_waitcnt lgkmcnt(1)
	v_mul_f32_e32 v36, v6, v36
	v_mul_f32_e32 v10, v6, v10
	v_mul_f32_e32 v78, v6, v78
	v_mul_f32_e32 v12, v6, v12
	v_mul_f32_e32 v18, v36, v18
	v_mul_f32_e32 v10, v10, v19
	v_mul_f32_e32 v14, v78, v14
	v_mul_f32_e32 v12, v12, v15
	v_cvt_pk_fp8_f32 v24, v18, v10
	v_cvt_pk_fp8_f32 v25, v14, v12
	v_lshlrev_b32_e32 v77, 16, v11
	v_and_b32_e32 v11, 0xffff0000, v11
	v_lshlrev_b32_e32 v79, 16, v13
	v_and_b32_e32 v13, 0xffff0000, v13
	v_mul_f32_e32 v77, v6, v77
	v_mul_f32_e32 v11, v6, v11
	v_mul_f32_e32 v79, v6, v79
	v_mul_f32_e32 v13, v6, v13
	v_mul_f32_e32 v19, v77, v20
	v_mul_f32_e32 v11, v11, v21
	v_mul_f32_e32 v10, v79, v16
	v_mul_f32_e32 v12, v13, v17
	v_cvt_pk_fp8_f32 v24, v19, v11 op_sel:[0,0,1]
	v_cvt_pk_fp8_f32 v25, v10, v12 op_sel:[0,0,1]
	global_load_dwordx4 v[10:13], v[22:23], off
	global_load_dwordx4 v[14:17], v[22:23], off offset:1024
	global_load_dwordx4 v[18:21], v[22:23], off offset:2048
	global_load_dwordx4 v[78:81], v[22:23], off offset:3072
	s_waitcnt vmcnt(6)
	v_lshlrev_b32_e32 v36, 16, v26
	v_and_b32_e32 v26, 0xffff0000, v26
	global_store_dwordx2 v[86:87], v[24:25], off
	v_mov_b64_e32 v[22:23], v[200:201]
	v_mov_b64_e32 v[24:25], v[202:203]
	s_nop 0
	v_mov_b64_e32 v[82:83], v[204:205]
	v_mov_b64_e32 v[84:85], v[206:207]
	v_lshlrev_b32_e32 v77, 16, v27
	v_and_b32_e32 v27, 0xffff0000, v27
	v_lshlrev_b32_e32 v90, 16, v28
	v_and_b32_e32 v28, 0xffff0000, v28
	v_mul_f32_e32 v36, v6, v36
	v_mul_f32_e32 v26, v6, v26
	v_mul_f32_e32 v27, v6, v27
	v_mul_f32_e32 v90, v6, v90
	v_mul_f32_e32 v28, v6, v28
	v_lshlrev_b32_e32 v91, 16, v29
	v_and_b32_e32 v29, 0xffff0000, v29
	v_mul_f32_e32 v77, v6, v77
	v_mul_f32_e32 v91, v6, v91
	v_mul_f32_e32 v29, v6, v29
	v_mul_f32_e32 v22, v36, v22
	v_mul_f32_e32 v23, v26, v23
	v_mul_f32_e32 v25, v27, v25
	v_mul_f32_e32 v26, v90, v82
	v_mul_f32_e32 v27, v28, v83
	v_cvt_pk_fp8_f32 v88, v22, v23
	v_cvt_pk_fp8_f32 v89, v26, v27
	v_mul_f32_e32 v24, v77, v24
	v_mul_f32_e32 v22, v91, v84
	v_mul_f32_e32 v23, v29, v85
	v_cvt_pk_fp8_f32 v88, v24, v25 op_sel:[0,0,1]
	v_cvt_pk_fp8_f32 v89, v22, v23 op_sel:[0,0,1]
	s_waitcnt vmcnt(6)
	v_lshlrev_b32_e32 v36, 16, v30
	v_and_b32_e32 v30, 0xffff0000, v30
	v_lshlrev_b32_e32 v84, 16, v32
	global_store_dwordx2 v[86:87], v[88:89], off offset:512
	v_mov_b64_e32 v[22:23], v[208:209]
	v_mov_b64_e32 v[24:25], v[210:211]
	v_mov_b64_e32 v[26:27], v[236:237]
	v_mov_b64_e32 v[28:29], v[238:239]
	v_and_b32_e32 v32, 0xffff0000, v32
	v_mul_f32_e32 v36, v6, v36
	v_mul_f32_e32 v30, v6, v30
	v_mul_f32_e32 v84, v6, v84
	v_mul_f32_e32 v32, v6, v32
	v_mov_b32_e32 v82, v37
	v_mov_b32_e32 v83, v37
	v_lshlrev_b32_e32 v77, 16, v31
	v_and_b32_e32 v31, 0xffff0000, v31
	v_lshlrev_b32_e32 v85, 16, v33
	v_and_b32_e32 v33, 0xffff0000, v33
	v_mul_f32_e32 v77, v6, v77
	v_mul_f32_e32 v31, v6, v31
	v_mul_f32_e32 v85, v6, v85
	v_mul_f32_e32 v33, v6, v33
	v_mov_b32_e32 v88, v37
	v_mov_b32_e32 v89, v37
	s_waitcnt vmcnt(4)
	v_lshlrev_b32_e32 v90, 16, v17
	v_and_b32_e32 v17, 0xffff0000, v17
	v_mul_f32_e32 v90, v7, v90
	v_mul_f32_e32 v17, v7, v17
	v_mul_f32_e32 v22, v36, v22
	v_mul_f32_e32 v23, v30, v23
	v_mul_f32_e32 v26, v84, v26
	v_mul_f32_e32 v27, v32, v27
	v_cvt_pk_fp8_f32 v82, v22, v23
	v_cvt_pk_fp8_f32 v83, v26, v27
	v_mul_f32_e32 v24, v77, v24
	v_mul_f32_e32 v25, v31, v25
	v_mul_f32_e32 v22, v85, v28
	v_mul_f32_e32 v23, v33, v29
	v_cvt_pk_fp8_f32 v82, v24, v25 op_sel:[0,0,1]
	v_cvt_pk_fp8_f32 v83, v22, v23 op_sel:[0,0,1]
	v_lshlrev_b32_e32 v32, 16, v58
	v_and_b32_e32 v33, 0xffff0000, v58
	v_lshlrev_b32_e32 v36, 16, v59
	global_store_dwordx2 v[86:87], v[82:83], off offset:1024
	v_mov_b64_e32 v[22:23], v[240:241]
	v_mov_b64_e32 v[24:25], v[242:243]
	v_mov_b64_e32 v[26:27], v[244:245]
	v_mov_b64_e32 v[28:29], v[246:247]
	v_and_b32_e32 v58, 0xffff0000, v59
	v_lshlrev_b32_e32 v59, 16, v60
	v_and_b32_e32 v60, 0xffff0000, v60
	v_mul_f32_e32 v32, v6, v32
	v_mul_f32_e32 v33, v6, v33
	v_mul_f32_e32 v59, v6, v59
	v_mul_f32_e32 v60, v6, v60
	v_mov_b32_e32 v30, v37
	v_mov_b32_e32 v31, v37
	v_lshlrev_b32_e32 v77, 16, v61
	v_and_b32_e32 v61, 0xffff0000, v61
	v_mul_f32_e32 v36, v6, v36
	v_mul_f32_e32 v58, v6, v58
	v_mul_f32_e32 v77, v6, v77
	v_mul_f32_e32 v6, v6, v61
	v_mul_f32_e32 v22, v32, v22
	v_mul_f32_e32 v23, v33, v23
	v_mul_f32_e32 v26, v59, v26
	v_mul_f32_e32 v27, v60, v27
	v_cvt_pk_fp8_f32 v30, v22, v23
	v_cvt_pk_fp8_f32 v31, v26, v27
	v_mul_f32_e32 v24, v36, v24
	v_mul_f32_e32 v25, v58, v25
	v_mul_f32_e32 v22, v77, v28
	v_mul_f32_e32 v6, v6, v29
	v_cvt_pk_fp8_f32 v30, v24, v25 op_sel:[0,0,1]
	v_cvt_pk_fp8_f32 v31, v22, v6 op_sel:[0,0,1]
	v_lshlrev_b32_e32 v6, 16, v10
	v_and_b32_e32 v10, 0xffff0000, v10
	v_lshlrev_b32_e32 v33, 16, v12
	global_store_dwordx2 v[86:87], v[30:31], off offset:1536
	v_mov_b64_e32 v[22:23], v[120:121]
	v_mov_b64_e32 v[24:25], v[122:123]
	v_mov_b64_e32 v[26:27], v[124:125]
	v_mov_b64_e32 v[28:29], v[126:127]
	v_and_b32_e32 v12, 0xffff0000, v12
	v_mul_f32_e32 v6, v7, v6
	v_mul_f32_e32 v10, v7, v10
	v_mul_f32_e32 v33, v7, v33
	v_mul_f32_e32 v12, v7, v12
	v_mov_b32_e32 v58, v37
	v_mov_b32_e32 v59, v37
	v_lshlrev_b32_e32 v32, 16, v11
	v_and_b32_e32 v11, 0xffff0000, v11
	v_lshlrev_b32_e32 v36, 16, v13
	v_and_b32_e32 v13, 0xffff0000, v13
	v_mul_f32_e32 v32, v7, v32
	v_mul_f32_e32 v11, v7, v11
	v_mul_f32_e32 v36, v7, v36
	v_mul_f32_e32 v13, v7, v13
	v_lshl_add_u64 v[30:31], v[40:41], 0, s[16:17]
	v_lshl_add_u64 v[86:87], v[44:45], 0, s[14:15]
	v_lshlrev_b32_e32 v77, 16, v16
	v_and_b32_e32 v16, 0xffff0000, v16
	v_mul_f32_e32 v77, v7, v77
	v_mul_f32_e32 v16, v7, v16
	s_add_i32 s14, s12, 3
	s_ashr_i32 s15, s14, 31
	s_lshl_b64 s[16:17], s[14:15], 12
	s_lshl_b64 s[14:15], s[14:15], 11
	v_mul_f32_e32 v6, v6, v22
	v_mul_f32_e32 v10, v10, v23
	v_mul_f32_e32 v23, v33, v26
	v_mul_f32_e32 v12, v12, v27
	v_cvt_pk_fp8_f32 v58, v6, v10
	v_cvt_pk_fp8_f32 v59, v23, v12
	v_mul_f32_e32 v22, v32, v24
	v_mul_f32_e32 v11, v11, v25
	v_mul_f32_e32 v6, v36, v28
	v_mul_f32_e32 v10, v13, v29
	v_cvt_pk_fp8_f32 v58, v22, v11 op_sel:[0,0,1]
	v_cvt_pk_fp8_f32 v59, v6, v10 op_sel:[0,0,1]
	global_load_dwordx4 v[10:13], v[30:31], off offset:3072
	global_load_dwordx4 v[22:25], v[30:31], off offset:2048
	global_load_dwordx4 v[26:29], v[30:31], off offset:1024
	s_nop 0
	global_load_dwordx4 v[30:33], v[30:31], off
	v_lshlrev_b32_e32 v6, 16, v14
	v_and_b32_e32 v14, 0xffff0000, v14
	global_store_dwordx2 v[86:87], v[58:59], off
	v_mov_b64_e32 v[58:59], v[200:201]
	v_mov_b64_e32 v[60:61], v[202:203]
	s_nop 0
	v_mov_b64_e32 v[82:83], v[204:205]
	v_mov_b64_e32 v[84:85], v[206:207]
	v_mul_f32_e32 v6, v7, v6
	v_mul_f32_e32 v14, v7, v14
	v_lshlrev_b32_e32 v36, 16, v15
	v_and_b32_e32 v15, 0xffff0000, v15
	v_mul_f32_e32 v36, v7, v36
	v_mul_f32_e32 v15, v7, v15
	v_mul_f32_e32 v6, v6, v58
	v_mul_f32_e32 v14, v14, v59
	v_mul_f32_e32 v58, v77, v82
	v_mul_f32_e32 v16, v16, v83
	v_cvt_pk_fp8_f32 v88, v6, v14
	v_cvt_pk_fp8_f32 v89, v58, v16
	v_mul_f32_e32 v36, v36, v60
	v_mul_f32_e32 v15, v15, v61
	v_mul_f32_e32 v6, v90, v84
	v_mul_f32_e32 v14, v17, v85
	v_cvt_pk_fp8_f32 v88, v36, v15 op_sel:[0,0,1]
	v_cvt_pk_fp8_f32 v89, v6, v14 op_sel:[0,0,1]
	s_waitcnt vmcnt(10)
	v_lshlrev_b32_e32 v6, 16, v18
	v_and_b32_e32 v18, 0xffff0000, v18
	v_lshlrev_b32_e32 v36, 16, v19
	global_store_dwordx2 v[86:87], v[88:89], off offset:512
	v_mov_b64_e32 v[14:15], v[208:209]
	v_mov_b64_e32 v[16:17], v[210:211]
	v_mov_b64_e32 v[58:59], v[236:237]
	v_mov_b64_e32 v[60:61], v[238:239]
	v_and_b32_e32 v19, 0xffff0000, v19
	v_lshlrev_b32_e32 v77, 16, v20
	v_and_b32_e32 v20, 0xffff0000, v20
	v_mul_f32_e32 v6, v7, v6
	v_mul_f32_e32 v18, v7, v18
	v_mul_f32_e32 v36, v7, v36
	v_mul_f32_e32 v19, v7, v19
	v_mul_f32_e32 v77, v7, v77
	v_mul_f32_e32 v20, v7, v20
	v_mov_b32_e32 v82, v37
	v_mov_b32_e32 v83, v37
	v_lshlrev_b32_e32 v84, 16, v21
	v_and_b32_e32 v21, 0xffff0000, v21
	v_mul_f32_e32 v84, v7, v84
	v_mul_f32_e32 v21, v7, v21
	s_waitcnt vmcnt(3)
	v_lshlrev_b32_e32 v88, 16, v28
	v_and_b32_e32 v28, 0xffff0000, v28
	v_mul_f32_e32 v88, v8, v88
	v_mul_f32_e32 v28, v8, v28
	v_lshlrev_b32_e32 v89, 16, v29
	v_and_b32_e32 v29, 0xffff0000, v29
	v_mul_f32_e32 v89, v8, v89
	v_mul_f32_e32 v29, v8, v29
	v_mul_f32_e32 v6, v6, v14
	v_mul_f32_e32 v14, v18, v15
	v_mul_f32_e32 v15, v36, v16
	v_mul_f32_e32 v16, v19, v17
	v_mul_f32_e32 v17, v77, v58
	v_mul_f32_e32 v18, v20, v59
	v_cvt_pk_fp8_f32 v82, v6, v14
	v_cvt_pk_fp8_f32 v83, v17, v18
	v_mul_f32_e32 v6, v84, v60
	v_mul_f32_e32 v14, v21, v61
	v_cvt_pk_fp8_f32 v82, v15, v16 op_sel:[0,0,1]
	v_cvt_pk_fp8_f32 v83, v6, v14 op_sel:[0,0,1]
	v_lshlrev_b32_e32 v6, 16, v78
	v_and_b32_e32 v36, 0xffff0000, v78
	v_lshlrev_b32_e32 v60, 16, v79
	global_store_dwordx2 v[86:87], v[82:83], off offset:1024
	v_mov_b64_e32 v[14:15], v[240:241]
	v_mov_b64_e32 v[16:17], v[242:243]
	v_mov_b64_e32 v[18:19], v[244:245]
	v_mov_b64_e32 v[20:21], v[246:247]
	v_and_b32_e32 v61, 0xffff0000, v79
	v_lshlrev_b32_e32 v77, 16, v80
	v_and_b32_e32 v78, 0xffff0000, v80
	v_mul_f32_e32 v6, v7, v6
	v_mul_f32_e32 v36, v7, v36
	v_mul_f32_e32 v60, v7, v60
	v_mul_f32_e32 v61, v7, v61
	v_mul_f32_e32 v77, v7, v77
	v_mul_f32_e32 v78, v7, v78
	v_mov_b32_e32 v58, v37
	v_mov_b32_e32 v59, v37
	v_lshlrev_b32_e32 v79, 16, v81
	v_and_b32_e32 v80, 0xffff0000, v81
	v_mul_f32_e32 v79, v7, v79
	v_mul_f32_e32 v7, v7, v80
	v_mul_f32_e32 v6, v6, v14
	v_mul_f32_e32 v14, v36, v15
	v_mul_f32_e32 v15, v60, v16
	v_mul_f32_e32 v16, v61, v17
	v_mul_f32_e32 v17, v77, v18
	v_mul_f32_e32 v18, v78, v19
	v_cvt_pk_fp8_f32 v58, v6, v14
	v_cvt_pk_fp8_f32 v59, v17, v18
	v_mul_f32_e32 v6, v79, v20
	v_mul_f32_e32 v7, v7, v21
	v_cvt_pk_fp8_f32 v58, v15, v16 op_sel:[0,0,1]
	v_cvt_pk_fp8_f32 v59, v6, v7 op_sel:[0,0,1]
	s_waitcnt vmcnt(3)
	v_lshlrev_b32_e32 v36, 16, v30
	v_and_b32_e32 v30, 0xffff0000, v30
	v_mul_f32_e32 v36, v8, v36
	global_store_dwordx2 v[86:87], v[58:59], off offset:1536
	v_mov_b64_e32 v[14:15], v[120:121]
	v_mov_b64_e32 v[16:17], v[122:123]
	v_mov_b64_e32 v[18:19], v[124:125]
	v_mov_b64_e32 v[20:21], v[126:127]
	v_lshlrev_b32_e32 v59, 16, v32
	v_and_b32_e32 v32, 0xffff0000, v32
	v_mul_f32_e32 v30, v8, v30
	v_mul_f32_e32 v59, v8, v59
	v_mul_f32_e32 v32, v8, v32
	v_mov_b32_e32 v6, v37
	v_mov_b32_e32 v7, v37
	v_lshlrev_b32_e32 v58, 16, v31
	v_and_b32_e32 v31, 0xffff0000, v31
	v_lshlrev_b32_e32 v60, 16, v33
	v_and_b32_e32 v33, 0xffff0000, v33
	v_mul_f32_e32 v58, v8, v58
	v_mul_f32_e32 v31, v8, v31
	v_mul_f32_e32 v60, v8, v60
	v_mul_f32_e32 v33, v8, v33
	v_lshl_add_u64 v[78:79], v[40:41], 0, s[16:17]
	v_lshl_add_u64 v[86:87], v[44:45], 0, s[2:3]
	v_lshlrev_b32_e32 v77, 16, v27
	v_and_b32_e32 v27, 0xffff0000, v27
	v_mul_f32_e32 v27, v8, v27
	v_mul_f32_e32 v77, v8, v77
	s_add_i32 s2, s12, 4
	s_ashr_i32 s3, s2, 31
	s_lshl_b64 s[16:17], s[2:3], 12
	s_lshl_b64 s[2:3], s[2:3], 11
	v_mul_f32_e32 v14, v36, v14
	v_mul_f32_e32 v15, v30, v15
	v_mul_f32_e32 v18, v59, v18
	v_mul_f32_e32 v19, v32, v19
	v_cvt_pk_fp8_f32 v6, v14, v15
	v_cvt_pk_fp8_f32 v7, v18, v19
	v_mul_f32_e32 v16, v58, v16
	v_mul_f32_e32 v17, v31, v17
	v_mul_f32_e32 v14, v60, v20
	v_mul_f32_e32 v15, v33, v21
	v_cvt_pk_fp8_f32 v6, v16, v17 op_sel:[0,0,1]
	v_cvt_pk_fp8_f32 v7, v14, v15 op_sel:[0,0,1]
	global_load_dwordx4 v[14:17], v[78:79], off
	global_load_dwordx4 v[30:33], v[78:79], off offset:1024
	global_load_dwordx4 v[58:61], v[78:79], off offset:2048
	s_nop 0
	global_load_dwordx4 v[78:81], v[78:79], off offset:3072
	v_lshlrev_b32_e32 v36, 16, v26
	v_and_b32_e32 v26, 0xffff0000, v26
	global_store_dwordx2 v[86:87], v[6:7], off
	v_mov_b64_e32 v[18:19], v[200:201]
	v_mov_b64_e32 v[20:21], v[202:203]
	v_mov_b64_e32 v[82:83], v[204:205]
	v_mov_b64_e32 v[84:85], v[206:207]
	v_mul_f32_e32 v36, v8, v36
	v_mul_f32_e32 v26, v8, v26
	v_mov_b32_e32 v6, v37
	v_mov_b32_e32 v7, v37
	v_mul_f32_e32 v18, v36, v18
	v_mul_f32_e32 v19, v26, v19
	v_mul_f32_e32 v21, v27, v21
	v_mul_f32_e32 v26, v88, v82
	v_mul_f32_e32 v27, v28, v83
	v_cvt_pk_fp8_f32 v6, v18, v19
	v_cvt_pk_fp8_f32 v7, v26, v27
	v_mul_f32_e32 v20, v77, v20
	v_mul_f32_e32 v18, v89, v84
	v_mul_f32_e32 v19, v29, v85
	v_cvt_pk_fp8_f32 v6, v20, v21 op_sel:[0,0,1]
	v_cvt_pk_fp8_f32 v7, v18, v19 op_sel:[0,0,1]
	v_lshlrev_b32_e32 v36, 16, v22
	v_and_b32_e32 v22, 0xffff0000, v22
	v_lshlrev_b32_e32 v77, 16, v23
	global_store_dwordx2 v[86:87], v[6:7], off offset:512
	v_mov_b64_e32 v[18:19], v[208:209]
	v_mov_b64_e32 v[20:21], v[210:211]
	v_mov_b64_e32 v[26:27], v[236:237]
	v_mov_b64_e32 v[28:29], v[238:239]
	v_and_b32_e32 v23, 0xffff0000, v23
	v_lshlrev_b32_e32 v82, 16, v24
	v_and_b32_e32 v24, 0xffff0000, v24
	v_mul_f32_e32 v36, v8, v36
	v_mul_f32_e32 v22, v8, v22
	v_mul_f32_e32 v23, v8, v23
	v_mul_f32_e32 v82, v8, v82
	v_mul_f32_e32 v24, v8, v24
	v_mov_b32_e32 v6, v37
	v_mov_b32_e32 v7, v37
	v_lshlrev_b32_e32 v83, 16, v25
	v_and_b32_e32 v25, 0xffff0000, v25
	v_mul_f32_e32 v77, v8, v77
	v_mul_f32_e32 v83, v8, v83
	v_mul_f32_e32 v25, v8, v25
	s_waitcnt vmcnt(4)
	v_lshlrev_b32_e32 v88, 16, v33
	v_and_b32_e32 v33, 0xffff0000, v33
	v_mul_f32_e32 v88, v9, v88
	v_mul_f32_e32 v33, v9, v33
	v_mul_f32_e32 v18, v36, v18
	v_mul_f32_e32 v19, v22, v19
	v_mul_f32_e32 v21, v23, v21
	v_mul_f32_e32 v22, v82, v26
	v_mul_f32_e32 v23, v24, v27
	v_cvt_pk_fp8_f32 v6, v18, v19
	v_cvt_pk_fp8_f32 v7, v22, v23
	v_mul_f32_e32 v20, v77, v20
	v_mul_f32_e32 v18, v83, v28
	v_mul_f32_e32 v19, v25, v29
	v_cvt_pk_fp8_f32 v6, v20, v21 op_sel:[0,0,1]
	v_cvt_pk_fp8_f32 v7, v18, v19 op_sel:[0,0,1]
	v_lshlrev_b32_e32 v26, 16, v10
	v_and_b32_e32 v10, 0xffff0000, v10
	v_lshlrev_b32_e32 v28, 16, v12
	global_store_dwordx2 v[86:87], v[6:7], off offset:1024
	v_mov_b64_e32 v[18:19], v[240:241]
	v_mov_b64_e32 v[20:21], v[242:243]
	v_mov_b64_e32 v[22:23], v[244:245]
	v_mov_b64_e32 v[24:25], v[246:247]
	v_and_b32_e32 v12, 0xffff0000, v12
	v_lshlrev_b32_e32 v27, 16, v11
	v_and_b32_e32 v11, 0xffff0000, v11
	v_lshlrev_b32_e32 v29, 16, v13
	v_and_b32_e32 v13, 0xffff0000, v13
	v_mul_f32_e32 v26, v8, v26
	v_mul_f32_e32 v10, v8, v10
	v_mul_f32_e32 v28, v8, v28
	v_mul_f32_e32 v12, v8, v12
	v_mov_b32_e32 v6, v37
	v_mov_b32_e32 v7, v37
	v_mul_f32_e32 v27, v8, v27
	v_mul_f32_e32 v11, v8, v11
	v_mul_f32_e32 v29, v8, v29
	v_mul_f32_e32 v8, v8, v13
	v_lshlrev_b32_e32 v36, 16, v31
	v_and_b32_e32 v31, 0xffff0000, v31
	v_lshlrev_b32_e32 v77, 16, v32
	v_and_b32_e32 v32, 0xffff0000, v32
	v_mul_f32_e32 v36, v9, v36
	v_mul_f32_e32 v31, v9, v31
	v_mul_f32_e32 v77, v9, v77
	v_mul_f32_e32 v32, v9, v32
	v_mul_f32_e32 v13, v26, v18
	v_mul_f32_e32 v10, v10, v19
	v_mul_f32_e32 v19, v28, v22
	v_mul_f32_e32 v12, v12, v23
	v_cvt_pk_fp8_f32 v6, v13, v10
	v_cvt_pk_fp8_f32 v7, v19, v12
	v_mul_f32_e32 v18, v27, v20
	v_mul_f32_e32 v11, v11, v21
	v_mul_f32_e32 v10, v29, v24
	v_mul_f32_e32 v8, v8, v25
	v_cvt_pk_fp8_f32 v6, v18, v11 op_sel:[0,0,1]
	v_cvt_pk_fp8_f32 v7, v10, v8 op_sel:[0,0,1]
	v_lshlrev_b32_e32 v8, 16, v14
	v_and_b32_e32 v14, 0xffff0000, v14
	v_lshlrev_b32_e32 v24, 16, v15
	global_store_dwordx2 v[86:87], v[6:7], off offset:1536
	v_mov_b64_e32 v[10:11], v[120:121]
	v_mov_b64_e32 v[12:13], v[122:123]
	v_mov_b64_e32 v[18:19], v[124:125]
	v_mov_b64_e32 v[20:21], v[126:127]
	v_and_b32_e32 v15, 0xffff0000, v15
	v_lshlrev_b32_e32 v25, 16, v16
	v_and_b32_e32 v16, 0xffff0000, v16
	v_mul_f32_e32 v8, v9, v8
	v_mul_f32_e32 v14, v9, v14
	v_mul_f32_e32 v24, v9, v24
	v_mul_f32_e32 v15, v9, v15
	v_mul_f32_e32 v25, v9, v25
	v_mul_f32_e32 v16, v9, v16
	v_mov_b32_e32 v6, v37
	v_mov_b32_e32 v7, v37
	v_lshlrev_b32_e32 v26, 16, v17
	v_and_b32_e32 v17, 0xffff0000, v17
	v_mul_f32_e32 v26, v9, v26
	v_mul_f32_e32 v17, v9, v17
	v_lshl_add_u64 v[22:23], v[40:41], 0, s[16:17]
	v_lshl_add_u64 v[86:87], v[44:45], 0, s[14:15]
	s_add_i32 s14, s12, 5
	s_ashr_i32 s15, s14, 31
	s_lshl_b64 s[16:17], s[14:15], 12
	s_lshl_b64 s[14:15], s[14:15], 11
	v_mul_f32_e32 v8, v8, v10
	v_mul_f32_e32 v10, v14, v11
	v_mul_f32_e32 v11, v24, v12
	v_mul_f32_e32 v12, v15, v13
	v_mul_f32_e32 v13, v25, v18
	v_mul_f32_e32 v14, v16, v19
	v_cvt_pk_fp8_f32 v6, v8, v10
	v_cvt_pk_fp8_f32 v7, v13, v14
	v_mul_f32_e32 v8, v26, v20
	v_mul_f32_e32 v10, v17, v21
	v_cvt_pk_fp8_f32 v6, v11, v12 op_sel:[0,0,1]
	v_cvt_pk_fp8_f32 v7, v8, v10 op_sel:[0,0,1]
	global_load_dwordx4 v[10:13], v[22:23], off offset:3072
	global_load_dwordx4 v[18:21], v[22:23], off offset:2048
	global_load_dwordx4 v[82:85], v[22:23], off offset:1024
	global_load_dwordx4 v[14:17], v[22:23], off
	v_lshlrev_b32_e32 v8, 16, v30
	v_and_b32_e32 v30, 0xffff0000, v30
	global_store_dwordx2 v[86:87], v[6:7], off
	v_mov_b64_e32 v[22:23], v[200:201]
	v_mov_b64_e32 v[24:25], v[202:203]
	v_mov_b64_e32 v[26:27], v[204:205]
	v_mov_b64_e32 v[28:29], v[206:207]
	v_mul_f32_e32 v8, v9, v8
	v_mul_f32_e32 v30, v9, v30
	v_mov_b32_e32 v6, v37
	v_mov_b32_e32 v7, v37
	v_mul_f32_e32 v8, v8, v22
	v_mul_f32_e32 v22, v30, v23
	v_mul_f32_e32 v23, v36, v24
	v_mul_f32_e32 v24, v31, v25
	v_mul_f32_e32 v25, v77, v26
	v_mul_f32_e32 v26, v32, v27
	v_cvt_pk_fp8_f32 v6, v8, v22
	v_cvt_pk_fp8_f32 v7, v25, v26
	v_mul_f32_e32 v8, v88, v28
	v_mul_f32_e32 v22, v33, v29
	v_cvt_pk_fp8_f32 v6, v23, v24 op_sel:[0,0,1]
	v_cvt_pk_fp8_f32 v7, v8, v22 op_sel:[0,0,1]
	s_waitcnt vmcnt(10)
	v_lshlrev_b32_e32 v8, 16, v58
	v_and_b32_e32 v30, 0xffff0000, v58
	v_lshlrev_b32_e32 v31, 16, v59
	global_store_dwordx2 v[86:87], v[6:7], off offset:512
	v_mov_b64_e32 v[22:23], v[208:209]
	v_mov_b64_e32 v[24:25], v[210:211]
	v_mov_b64_e32 v[26:27], v[236:237]
	v_mov_b64_e32 v[28:29], v[238:239]
	v_and_b32_e32 v32, 0xffff0000, v59
	v_lshlrev_b32_e32 v33, 16, v60
	v_and_b32_e32 v36, 0xffff0000, v60
	v_mul_f32_e32 v8, v9, v8
	v_mul_f32_e32 v30, v9, v30
	v_mul_f32_e32 v31, v9, v31
	v_mul_f32_e32 v32, v9, v32
	v_mul_f32_e32 v33, v9, v33
	v_mul_f32_e32 v36, v9, v36
	v_mov_b32_e32 v6, v37
	v_mov_b32_e32 v7, v37
	v_lshlrev_b32_e32 v58, 16, v61
	v_and_b32_e32 v59, 0xffff0000, v61
	v_mul_f32_e32 v58, v9, v58
	v_mul_f32_e32 v59, v9, v59
	s_waitcnt vmcnt(3)
	v_and_b32_e32 v77, 0xffff0000, v82
	s_waitcnt lgkmcnt(0)
	v_mul_f32_e32 v77, v2, v77
	v_mul_f32_e32 v8, v8, v22
	v_mul_f32_e32 v22, v30, v23
	v_mul_f32_e32 v23, v31, v24
	v_mul_f32_e32 v24, v32, v25
	v_mul_f32_e32 v25, v33, v26
	v_mul_f32_e32 v26, v36, v27
	v_cvt_pk_fp8_f32 v6, v8, v22
	v_cvt_pk_fp8_f32 v7, v25, v26
	v_mul_f32_e32 v8, v58, v28
	v_mul_f32_e32 v22, v59, v29
	v_cvt_pk_fp8_f32 v6, v23, v24 op_sel:[0,0,1]
	v_cvt_pk_fp8_f32 v7, v8, v22 op_sel:[0,0,1]
	v_lshlrev_b32_e32 v8, 16, v78
	v_and_b32_e32 v30, 0xffff0000, v78
	v_lshlrev_b32_e32 v31, 16, v79
	global_store_dwordx2 v[86:87], v[6:7], off offset:1024
	v_mov_b64_e32 v[22:23], v[240:241]
	v_mov_b64_e32 v[24:25], v[242:243]
	v_mov_b64_e32 v[26:27], v[244:245]
	v_mov_b64_e32 v[28:29], v[246:247]
	v_and_b32_e32 v32, 0xffff0000, v79
	v_lshlrev_b32_e32 v33, 16, v80
	v_and_b32_e32 v36, 0xffff0000, v80
	v_mul_f32_e32 v8, v9, v8
	v_mul_f32_e32 v30, v9, v30
	v_mul_f32_e32 v31, v9, v31
	v_mul_f32_e32 v32, v9, v32
	v_mul_f32_e32 v33, v9, v33
	v_mul_f32_e32 v36, v9, v36
	v_mov_b32_e32 v6, v37
	v_mov_b32_e32 v7, v37
	v_lshlrev_b32_e32 v58, 16, v81
	v_and_b32_e32 v59, 0xffff0000, v81
	v_mul_f32_e32 v58, v9, v58
	v_mul_f32_e32 v9, v9, v59
	v_lshl_add_u64 v[78:79], v[44:45], 0, s[2:3]
	v_mov_b32_e32 v80, v37
	v_mov_b32_e32 v81, v37
	v_mul_f32_e32 v8, v8, v22
	v_mul_f32_e32 v22, v30, v23
	v_mul_f32_e32 v23, v31, v24
	v_mul_f32_e32 v24, v32, v25
	v_mul_f32_e32 v25, v33, v26
	v_mul_f32_e32 v26, v36, v27
	v_cvt_pk_fp8_f32 v6, v8, v22
	v_cvt_pk_fp8_f32 v7, v25, v26
	v_mul_f32_e32 v8, v58, v28
	v_mul_f32_e32 v9, v9, v29
	v_cvt_pk_fp8_f32 v6, v23, v24 op_sel:[0,0,1]
	v_cvt_pk_fp8_f32 v7, v8, v9 op_sel:[0,0,1]
	s_waitcnt vmcnt(3)
	v_lshlrev_b32_e32 v26, 16, v14
	v_and_b32_e32 v14, 0xffff0000, v14
	v_lshlrev_b32_e32 v27, 16, v15
	global_store_dwordx2 v[86:87], v[6:7], off offset:1536
	v_mov_b64_e32 v[6:7], v[120:121]
	v_mov_b64_e32 v[8:9], v[122:123]
	s_nop 0
	v_mov_b64_e32 v[22:23], v[124:125]
	v_mov_b64_e32 v[24:25], v[126:127]
	v_and_b32_e32 v15, 0xffff0000, v15
	v_lshlrev_b32_e32 v28, 16, v16
	v_and_b32_e32 v16, 0xffff0000, v16
	v_mul_f32_e32 v26, v2, v26
	v_mul_f32_e32 v14, v2, v14
	v_mul_f32_e32 v15, v2, v15
	v_mul_f32_e32 v28, v2, v28
	v_mul_f32_e32 v16, v2, v16
	v_mov_b32_e32 v30, v37
	v_mov_b32_e32 v31, v37
	v_lshlrev_b32_e32 v29, 16, v17
	v_and_b32_e32 v17, 0xffff0000, v17
	v_mul_f32_e32 v27, v2, v27
	v_mul_f32_e32 v29, v2, v29
	v_mul_f32_e32 v17, v2, v17
	v_lshl_add_u64 v[32:33], v[40:41], 0, s[16:17]
	v_lshlrev_b32_e32 v36, 16, v82
	v_lshlrev_b32_e32 v86, 16, v84
	v_and_b32_e32 v84, 0xffff0000, v84
	v_mul_f32_e32 v36, v2, v36
	v_mul_f32_e32 v86, v2, v86
	v_mul_f32_e32 v84, v2, v84
	v_lshlrev_b32_e32 v82, 16, v83
	v_and_b32_e32 v83, 0xffff0000, v83
	v_lshlrev_b32_e32 v87, 16, v85
	v_and_b32_e32 v85, 0xffff0000, v85
	v_mul_f32_e32 v82, v2, v82
	v_mul_f32_e32 v83, v2, v83
	v_mul_f32_e32 v87, v2, v87
	v_mul_f32_e32 v85, v2, v85
	s_add_i32 s16, s12, 6
	s_ashr_i32 s17, s16, 31
	s_lshl_b64 s[2:3], s[16:17], 12
	s_add_i32 s12, s12, 7
	s_ashr_i32 s13, s12, 31
	v_mul_f32_e32 v6, v26, v6
	v_mul_f32_e32 v7, v14, v7
	v_mul_f32_e32 v9, v15, v9
	v_mul_f32_e32 v14, v28, v22
	v_mul_f32_e32 v15, v16, v23
	v_cvt_pk_fp8_f32 v30, v6, v7
	v_cvt_pk_fp8_f32 v31, v14, v15
	v_mul_f32_e32 v8, v27, v8
	v_mul_f32_e32 v6, v29, v24
	v_mul_f32_e32 v7, v17, v25
	v_cvt_pk_fp8_f32 v30, v8, v9 op_sel:[0,0,1]
	v_cvt_pk_fp8_f32 v31, v6, v7 op_sel:[0,0,1]
	global_load_dwordx4 v[26:29], v[32:33], off
	global_load_dwordx4 v[22:25], v[32:33], off offset:1024
	global_load_dwordx4 v[14:17], v[32:33], off offset:2048
	global_load_dwordx4 v[6:9], v[32:33], off offset:3072
	s_nop 0
	global_store_dwordx2 v[78:79], v[30:31], off
	v_mov_b64_e32 v[30:31], v[200:201]
	v_mov_b64_e32 v[32:33], v[202:203]
	s_nop 0
	v_mov_b64_e32 v[58:59], v[204:205]
	v_mov_b64_e32 v[60:61], v[206:207]
	v_mul_f32_e32 v30, v36, v30
	v_mul_f32_e32 v31, v77, v31
	v_mul_f32_e32 v36, v86, v58
	v_mul_f32_e32 v58, v84, v59
	v_cvt_pk_fp8_f32 v80, v30, v31
	v_cvt_pk_fp8_f32 v81, v36, v58
	v_mul_f32_e32 v32, v82, v32
	v_mul_f32_e32 v33, v83, v33
	v_mul_f32_e32 v30, v87, v60
	v_mul_f32_e32 v31, v85, v61
	v_cvt_pk_fp8_f32 v80, v32, v33 op_sel:[0,0,1]
	v_cvt_pk_fp8_f32 v81, v30, v31 op_sel:[0,0,1]
	v_lshlrev_b32_e32 v36, 16, v18
	v_and_b32_e32 v18, 0xffff0000, v18
	v_lshlrev_b32_e32 v77, 16, v19
	global_store_dwordx2 v[78:79], v[80:81], off offset:512
	v_mov_b64_e32 v[30:31], v[208:209]
	v_mov_b64_e32 v[32:33], v[210:211]
	v_mov_b64_e32 v[58:59], v[236:237]
	v_mov_b64_e32 v[60:61], v[238:239]
	v_lshlrev_b32_e32 v82, 16, v20
	v_and_b32_e32 v20, 0xffff0000, v20
	v_mul_f32_e32 v36, v2, v36
	v_mul_f32_e32 v18, v2, v18
	v_mul_f32_e32 v77, v2, v77
	v_mul_f32_e32 v82, v2, v82
	v_mul_f32_e32 v20, v2, v20
	v_mov_b32_e32 v80, v37
	v_mov_b32_e32 v81, v37
	v_and_b32_e32 v19, 0xffff0000, v19
	v_lshlrev_b32_e32 v83, 16, v21
	v_and_b32_e32 v21, 0xffff0000, v21
	v_mul_f32_e32 v19, v2, v19
	v_mul_f32_e32 v83, v2, v83
	v_mul_f32_e32 v21, v2, v21
	v_mov_b32_e32 v84, v37
	v_mov_b32_e32 v85, v37
	s_waitcnt vmcnt(4)
	v_lshlrev_b32_e32 v86, 16, v25
	v_and_b32_e32 v25, 0xffff0000, v25
	v_mul_f32_e32 v86, v3, v86
	v_mul_f32_e32 v25, v3, v25
	v_mul_f32_e32 v30, v36, v30
	v_mul_f32_e32 v18, v18, v31
	v_mul_f32_e32 v31, v77, v32
	v_mul_f32_e32 v32, v82, v58
	v_mul_f32_e32 v20, v20, v59
	v_cvt_pk_fp8_f32 v80, v30, v18
	v_cvt_pk_fp8_f32 v81, v32, v20
	v_mul_f32_e32 v19, v19, v33
	v_mul_f32_e32 v18, v83, v60
	v_mul_f32_e32 v20, v21, v61
	v_cvt_pk_fp8_f32 v80, v31, v19 op_sel:[0,0,1]
	v_cvt_pk_fp8_f32 v81, v18, v20 op_sel:[0,0,1]
	v_lshlrev_b32_e32 v36, 16, v10
	v_and_b32_e32 v10, 0xffff0000, v10
	v_lshlrev_b32_e32 v61, 16, v12
	global_store_dwordx2 v[78:79], v[80:81], off offset:1024
	v_mov_b64_e32 v[18:19], v[240:241]
	v_mov_b64_e32 v[20:21], v[242:243]
	v_mov_b64_e32 v[30:31], v[244:245]
	v_mov_b64_e32 v[32:33], v[246:247]
	v_and_b32_e32 v12, 0xffff0000, v12
	v_lshlrev_b32_e32 v60, 16, v11
	v_and_b32_e32 v11, 0xffff0000, v11
	v_lshlrev_b32_e32 v77, 16, v13
	v_and_b32_e32 v13, 0xffff0000, v13
	v_mul_f32_e32 v36, v2, v36
	v_mul_f32_e32 v10, v2, v10
	v_mul_f32_e32 v61, v2, v61
	v_mul_f32_e32 v12, v2, v12
	v_mov_b32_e32 v58, v37
	v_mov_b32_e32 v59, v37
	v_mul_f32_e32 v60, v2, v60
	v_mul_f32_e32 v11, v2, v11
	v_mul_f32_e32 v77, v2, v77
	v_mul_f32_e32 v2, v2, v13
	v_lshl_add_u64 v[82:83], v[44:45], 0, s[14:15]
	s_lshl_b64 s[14:15], s[16:17], 11
	v_mul_f32_e32 v13, v36, v18
	v_mul_f32_e32 v10, v10, v19
	v_mul_f32_e32 v19, v61, v30
	v_mul_f32_e32 v12, v12, v31
	v_cvt_pk_fp8_f32 v58, v13, v10
	v_cvt_pk_fp8_f32 v59, v19, v12
	v_mul_f32_e32 v18, v60, v20
	v_mul_f32_e32 v11, v11, v21
	v_mul_f32_e32 v10, v77, v32
	v_mul_f32_e32 v2, v2, v33
	v_cvt_pk_fp8_f32 v58, v18, v11 op_sel:[0,0,1]
	v_cvt_pk_fp8_f32 v59, v10, v2 op_sel:[0,0,1]
	v_lshlrev_b32_e32 v2, 16, v26
	v_and_b32_e32 v26, 0xffff0000, v26
	v_lshlrev_b32_e32 v30, 16, v27
	global_store_dwordx2 v[78:79], v[58:59], off offset:1536
	v_mov_b64_e32 v[10:11], v[120:121]
	v_mov_b64_e32 v[12:13], v[122:123]
	v_mov_b64_e32 v[18:19], v[124:125]
	v_mov_b64_e32 v[20:21], v[126:127]
	v_and_b32_e32 v27, 0xffff0000, v27
	v_lshlrev_b32_e32 v31, 16, v28
	v_and_b32_e32 v28, 0xffff0000, v28
	v_mul_f32_e32 v2, v3, v2
	v_mul_f32_e32 v26, v3, v26
	v_mul_f32_e32 v30, v3, v30
	v_mul_f32_e32 v27, v3, v27
	v_mul_f32_e32 v31, v3, v31
	v_mul_f32_e32 v28, v3, v28
	v_mov_b32_e32 v58, v37
	v_mov_b32_e32 v59, v37
	v_lshlrev_b32_e32 v32, 16, v29
	v_and_b32_e32 v29, 0xffff0000, v29
	v_mul_f32_e32 v32, v3, v32
	v_mul_f32_e32 v29, v3, v29
	v_lshl_add_u64 v[60:61], v[40:41], 0, s[2:3]
	v_lshlrev_b32_e32 v77, 16, v24
	v_and_b32_e32 v24, 0xffff0000, v24
	v_mul_f32_e32 v77, v3, v77
	v_mul_f32_e32 v24, v3, v24
	v_lshlrev_b32_e32 v36, 16, v23
	v_and_b32_e32 v23, 0xffff0000, v23
	v_mul_f32_e32 v36, v3, v36
	v_mul_f32_e32 v23, v3, v23
	s_lshl_b64 s[2:3], s[12:13], 12
	v_mul_f32_e32 v2, v2, v10
	v_mul_f32_e32 v10, v26, v11
	v_mul_f32_e32 v11, v30, v12
	v_mul_f32_e32 v12, v27, v13
	v_mul_f32_e32 v13, v31, v18
	v_mul_f32_e32 v18, v28, v19
	v_cvt_pk_fp8_f32 v58, v2, v10
	v_cvt_pk_fp8_f32 v59, v13, v18
	v_mul_f32_e32 v2, v32, v20
	v_mul_f32_e32 v10, v29, v21
	v_cvt_pk_fp8_f32 v58, v11, v12 op_sel:[0,0,1]
	v_cvt_pk_fp8_f32 v59, v2, v10 op_sel:[0,0,1]
	global_load_dwordx4 v[30:33], v[60:61], off
	global_load_dwordx4 v[26:29], v[60:61], off offset:1024
	global_load_dwordx4 v[18:21], v[60:61], off offset:2048
	global_load_dwordx4 v[10:13], v[60:61], off offset:3072
	v_lshlrev_b32_e32 v2, 16, v22
	v_and_b32_e32 v22, 0xffff0000, v22
	global_store_dwordx2 v[82:83], v[58:59], off
	v_mov_b64_e32 v[58:59], v[200:201]
	v_mov_b64_e32 v[60:61], v[202:203]
	s_nop 0
	v_mov_b64_e32 v[78:79], v[204:205]
	v_mov_b64_e32 v[80:81], v[206:207]
	v_mul_f32_e32 v2, v3, v2
	v_mul_f32_e32 v22, v3, v22
	v_mul_f32_e32 v2, v2, v58
	v_mul_f32_e32 v22, v22, v59
	v_mul_f32_e32 v58, v77, v78
	v_mul_f32_e32 v24, v24, v79
	v_cvt_pk_fp8_f32 v84, v2, v22
	v_cvt_pk_fp8_f32 v85, v58, v24
	v_mul_f32_e32 v36, v36, v60
	v_mul_f32_e32 v23, v23, v61
	v_mul_f32_e32 v2, v86, v80
	v_mul_f32_e32 v22, v25, v81
	v_cvt_pk_fp8_f32 v84, v36, v23 op_sel:[0,0,1]
	v_cvt_pk_fp8_f32 v85, v2, v22 op_sel:[0,0,1]
	s_waitcnt vmcnt(10)
	v_lshlrev_b32_e32 v2, 16, v14
	v_and_b32_e32 v14, 0xffff0000, v14
	v_lshlrev_b32_e32 v77, 16, v16
	global_store_dwordx2 v[82:83], v[84:85], off offset:512
	v_mov_b64_e32 v[22:23], v[208:209]
	v_mov_b64_e32 v[24:25], v[210:211]
	v_mov_b64_e32 v[58:59], v[236:237]
	v_mov_b64_e32 v[60:61], v[238:239]
	v_and_b32_e32 v16, 0xffff0000, v16
	v_mul_f32_e32 v2, v3, v2
	v_mul_f32_e32 v14, v3, v14
	v_mul_f32_e32 v77, v3, v77
	v_mul_f32_e32 v16, v3, v16
	v_mov_b32_e32 v78, v37
	v_mov_b32_e32 v79, v37
	v_lshlrev_b32_e32 v36, 16, v15
	v_and_b32_e32 v15, 0xffff0000, v15
	v_lshlrev_b32_e32 v80, 16, v17
	v_and_b32_e32 v17, 0xffff0000, v17
	v_mul_f32_e32 v36, v3, v36
	v_mul_f32_e32 v15, v3, v15
	v_mul_f32_e32 v80, v3, v80
	v_mul_f32_e32 v17, v3, v17
	s_waitcnt vmcnt(4)
	v_lshlrev_b32_e32 v84, 16, v28
	v_and_b32_e32 v28, 0xffff0000, v28
	v_mul_f32_e32 v84, v4, v84
	v_mul_f32_e32 v28, v4, v28
	v_lshlrev_b32_e32 v85, 16, v29
	v_and_b32_e32 v29, 0xffff0000, v29
	v_mul_f32_e32 v85, v4, v85
	v_mul_f32_e32 v29, v4, v29
	v_mul_f32_e32 v2, v2, v22
	v_mul_f32_e32 v14, v14, v23
	v_mul_f32_e32 v23, v77, v58
	v_mul_f32_e32 v16, v16, v59
	v_cvt_pk_fp8_f32 v78, v2, v14
	v_cvt_pk_fp8_f32 v79, v23, v16
	v_mul_f32_e32 v22, v36, v24
	v_mul_f32_e32 v15, v15, v25
	v_mul_f32_e32 v2, v80, v60
	v_mul_f32_e32 v14, v17, v61
	v_cvt_pk_fp8_f32 v78, v22, v15 op_sel:[0,0,1]
	v_cvt_pk_fp8_f32 v79, v2, v14 op_sel:[0,0,1]
	v_lshlrev_b32_e32 v2, 16, v6
	v_and_b32_e32 v6, 0xffff0000, v6
	v_lshlrev_b32_e32 v60, 16, v8
	global_store_dwordx2 v[82:83], v[78:79], off offset:1024
	v_mov_b64_e32 v[14:15], v[240:241]
	v_mov_b64_e32 v[16:17], v[242:243]
	v_mov_b64_e32 v[22:23], v[244:245]
	v_mov_b64_e32 v[24:25], v[246:247]
	v_and_b32_e32 v8, 0xffff0000, v8
	v_mul_f32_e32 v2, v3, v2
	v_mul_f32_e32 v6, v3, v6
	v_mul_f32_e32 v60, v3, v60
	v_mul_f32_e32 v8, v3, v8
	v_mov_b32_e32 v58, v37
	v_mov_b32_e32 v59, v37
	v_lshlrev_b32_e32 v36, 16, v7
	v_and_b32_e32 v7, 0xffff0000, v7
	v_lshlrev_b32_e32 v61, 16, v9
	v_and_b32_e32 v9, 0xffff0000, v9
	v_mul_f32_e32 v36, v3, v36
	v_mul_f32_e32 v7, v3, v7
	v_mul_f32_e32 v61, v3, v61
	v_mul_f32_e32 v3, v3, v9
	v_lshlrev_b32_e32 v77, 16, v27
	v_and_b32_e32 v27, 0xffff0000, v27
	v_mul_f32_e32 v77, v4, v77
	v_mul_f32_e32 v27, v4, v27
	v_mul_f32_e32 v2, v2, v14
	v_mul_f32_e32 v6, v6, v15
	v_mul_f32_e32 v14, v60, v22
	v_mul_f32_e32 v8, v8, v23
	v_cvt_pk_fp8_f32 v58, v2, v6
	v_cvt_pk_fp8_f32 v59, v14, v8
	v_mul_f32_e32 v9, v36, v16
	v_mul_f32_e32 v7, v7, v17
	v_mul_f32_e32 v2, v61, v24
	v_mul_f32_e32 v3, v3, v25
	v_cvt_pk_fp8_f32 v58, v9, v7 op_sel:[0,0,1]
	v_cvt_pk_fp8_f32 v59, v2, v3 op_sel:[0,0,1]
	v_lshlrev_b32_e32 v22, 16, v30
	v_and_b32_e32 v23, 0xffff0000, v30
	v_lshlrev_b32_e32 v24, 16, v31
	global_store_dwordx2 v[82:83], v[58:59], off offset:1536
	v_mov_b64_e32 v[6:7], v[120:121]
	v_mov_b64_e32 v[8:9], v[122:123]
	v_mov_b64_e32 v[14:15], v[124:125]
	v_mov_b64_e32 v[16:17], v[126:127]
	v_and_b32_e32 v25, 0xffff0000, v31
	v_lshlrev_b32_e32 v30, 16, v32
	v_and_b32_e32 v31, 0xffff0000, v32
	v_mul_f32_e32 v22, v4, v22
	v_mul_f32_e32 v23, v4, v23
	v_mul_f32_e32 v30, v4, v30
	v_mul_f32_e32 v31, v4, v31
	v_mov_b32_e32 v2, v37
	v_mov_b32_e32 v3, v37
	v_lshlrev_b32_e32 v32, 16, v33
	v_and_b32_e32 v33, 0xffff0000, v33
	v_mul_f32_e32 v24, v4, v24
	v_mul_f32_e32 v25, v4, v25
	v_mul_f32_e32 v32, v4, v32
	v_mul_f32_e32 v33, v4, v33
	v_lshl_add_u64 v[58:59], v[40:41], 0, s[2:3]
	v_lshl_add_u64 v[82:83], v[44:45], 0, s[14:15]
	v_lshlrev_b32_e32 v36, 16, v26
	v_and_b32_e32 v26, 0xffff0000, v26
	v_mul_f32_e32 v36, v4, v36
	v_mul_f32_e32 v26, v4, v26
	s_lshl_b64 s[2:3], s[12:13], 11
	v_mul_f32_e32 v6, v22, v6
	v_mul_f32_e32 v7, v23, v7
	v_mul_f32_e32 v14, v30, v14
	v_mul_f32_e32 v15, v31, v15
	v_cvt_pk_fp8_f32 v2, v6, v7
	v_cvt_pk_fp8_f32 v3, v14, v15
	v_mul_f32_e32 v8, v24, v8
	v_mul_f32_e32 v9, v25, v9
	v_mul_f32_e32 v6, v32, v16
	v_mul_f32_e32 v7, v33, v17
	v_cvt_pk_fp8_f32 v2, v8, v9 op_sel:[0,0,1]
	v_cvt_pk_fp8_f32 v3, v6, v7 op_sel:[0,0,1]
	global_load_dwordx4 v[30:33], v[58:59], off
	global_load_dwordx4 v[22:25], v[58:59], off offset:1024
	global_load_dwordx4 v[14:17], v[58:59], off offset:2048
	global_load_dwordx4 v[6:9], v[58:59], off offset:3072
	s_nop 0
	global_store_dwordx2 v[82:83], v[2:3], off
	v_mov_b64_e32 v[58:59], v[200:201]
	v_mov_b64_e32 v[60:61], v[202:203]
	v_mov_b64_e32 v[78:79], v[204:205]
	v_mov_b64_e32 v[80:81], v[206:207]
	v_mov_b32_e32 v2, v37
	v_mov_b32_e32 v3, v37
	v_mul_f32_e32 v36, v36, v58
	v_mul_f32_e32 v26, v26, v59
	v_mul_f32_e32 v59, v84, v78
	v_mul_f32_e32 v28, v28, v79
	v_cvt_pk_fp8_f32 v2, v36, v26
	v_cvt_pk_fp8_f32 v3, v59, v28
	v_mul_f32_e32 v58, v77, v60
	v_mul_f32_e32 v27, v27, v61
	v_mul_f32_e32 v26, v85, v80
	v_mul_f32_e32 v28, v29, v81
	v_cvt_pk_fp8_f32 v2, v58, v27 op_sel:[0,0,1]
	v_cvt_pk_fp8_f32 v3, v26, v28 op_sel:[0,0,1]
	s_waitcnt vmcnt(10)
	v_lshlrev_b32_e32 v36, 16, v18
	v_and_b32_e32 v18, 0xffff0000, v18
	v_lshlrev_b32_e32 v77, 16, v19
	global_store_dwordx2 v[82:83], v[2:3], off offset:512
	v_mov_b64_e32 v[26:27], v[208:209]
	v_mov_b64_e32 v[28:29], v[210:211]
	v_mov_b64_e32 v[58:59], v[236:237]
	v_mov_b64_e32 v[60:61], v[238:239]
	v_lshlrev_b32_e32 v78, 16, v20
	v_and_b32_e32 v20, 0xffff0000, v20
	v_mul_f32_e32 v36, v4, v36
	v_mul_f32_e32 v18, v4, v18
	v_mul_f32_e32 v77, v4, v77
	v_mul_f32_e32 v78, v4, v78
	v_mul_f32_e32 v20, v4, v20
	v_mov_b32_e32 v2, v37
	v_mov_b32_e32 v3, v37
	v_and_b32_e32 v19, 0xffff0000, v19
	v_lshlrev_b32_e32 v79, 16, v21
	v_and_b32_e32 v21, 0xffff0000, v21
	v_mul_f32_e32 v19, v4, v19
	v_mul_f32_e32 v79, v4, v79
	v_mul_f32_e32 v21, v4, v21
	v_mul_f32_e32 v26, v36, v26
	v_mul_f32_e32 v18, v18, v27
	v_mul_f32_e32 v27, v77, v28
	v_mul_f32_e32 v28, v78, v58
	v_mul_f32_e32 v20, v20, v59
	v_cvt_pk_fp8_f32 v2, v26, v18
	v_cvt_pk_fp8_f32 v3, v28, v20
	v_mul_f32_e32 v19, v19, v29
	v_mul_f32_e32 v18, v79, v60
	v_mul_f32_e32 v20, v21, v61
	v_cvt_pk_fp8_f32 v2, v27, v19 op_sel:[0,0,1]
	v_cvt_pk_fp8_f32 v3, v18, v20 op_sel:[0,0,1]
	s_waitcnt vmcnt(10)
	v_lshlrev_b32_e32 v36, 16, v10
	v_and_b32_e32 v10, 0xffff0000, v10
	v_lshlrev_b32_e32 v59, 16, v12
	global_store_dwordx2 v[82:83], v[2:3], off offset:1024
	v_mov_b64_e32 v[18:19], v[240:241]
	v_mov_b64_e32 v[20:21], v[242:243]
	v_mov_b64_e32 v[26:27], v[244:245]
	v_mov_b64_e32 v[28:29], v[246:247]
	v_and_b32_e32 v12, 0xffff0000, v12
	v_lshlrev_b32_e32 v58, 16, v11
	v_and_b32_e32 v11, 0xffff0000, v11
	v_lshlrev_b32_e32 v60, 16, v13
	v_and_b32_e32 v13, 0xffff0000, v13
	v_mul_f32_e32 v36, v4, v36
	v_mul_f32_e32 v10, v4, v10
	v_mul_f32_e32 v59, v4, v59
	v_mul_f32_e32 v12, v4, v12
	v_mov_b32_e32 v2, v37
	v_mov_b32_e32 v3, v37
	v_mul_f32_e32 v58, v4, v58
	v_mul_f32_e32 v11, v4, v11
	v_mul_f32_e32 v60, v4, v60
	v_mul_f32_e32 v4, v4, v13
	v_mul_f32_e32 v13, v36, v18
	v_mul_f32_e32 v10, v10, v19
	v_mul_f32_e32 v19, v59, v26
	v_mul_f32_e32 v12, v12, v27
	v_cvt_pk_fp8_f32 v2, v13, v10
	v_cvt_pk_fp8_f32 v3, v19, v12
	v_mul_f32_e32 v18, v58, v20
	v_mul_f32_e32 v11, v11, v21
	v_mul_f32_e32 v10, v60, v28
	v_mul_f32_e32 v4, v4, v29
	v_cvt_pk_fp8_f32 v2, v18, v11 op_sel:[0,0,1]
	v_cvt_pk_fp8_f32 v3, v10, v4 op_sel:[0,0,1]
	s_waitcnt vmcnt(6)
	v_lshlrev_b32_e32 v4, 16, v30
	v_and_b32_e32 v26, 0xffff0000, v30
	v_lshlrev_b32_e32 v27, 16, v31
	global_store_dwordx2 v[82:83], v[2:3], off offset:1536
	v_mov_b64_e32 v[10:11], v[120:121]
	v_mov_b64_e32 v[12:13], v[122:123]
	v_mov_b64_e32 v[18:19], v[124:125]
	v_mov_b64_e32 v[20:21], v[126:127]
	v_and_b32_e32 v28, 0xffff0000, v31
	v_lshlrev_b32_e32 v29, 16, v32
	v_and_b32_e32 v30, 0xffff0000, v32
	v_mul_f32_e32 v4, v5, v4
	v_mul_f32_e32 v26, v5, v26
	v_mul_f32_e32 v27, v5, v27
	v_mul_f32_e32 v28, v5, v28
	v_mul_f32_e32 v29, v5, v29
	v_mul_f32_e32 v30, v5, v30
	v_mov_b32_e32 v2, v37
	v_mov_b32_e32 v3, v37
	v_lshlrev_b32_e32 v31, 16, v33
	v_and_b32_e32 v32, 0xffff0000, v33
	v_mul_f32_e32 v31, v5, v31
	v_mul_f32_e32 v32, v5, v32
	v_mul_f32_e32 v4, v4, v10
	v_mul_f32_e32 v10, v26, v11
	v_mul_f32_e32 v11, v27, v12
	v_mul_f32_e32 v12, v28, v13
	v_mul_f32_e32 v13, v29, v18
	v_mul_f32_e32 v18, v30, v19
	v_cvt_pk_fp8_f32 v2, v4, v10
	v_cvt_pk_fp8_f32 v3, v13, v18
	v_mul_f32_e32 v4, v31, v20
	v_mul_f32_e32 v10, v32, v21
	v_cvt_pk_fp8_f32 v2, v11, v12 op_sel:[0,0,1]
	v_cvt_pk_fp8_f32 v3, v4, v10 op_sel:[0,0,1]
	v_lshl_add_u64 v[26:27], v[44:45], 0, s[2:3]
	s_waitcnt vmcnt(6)
	v_lshlrev_b32_e32 v4, 16, v22
	v_and_b32_e32 v22, 0xffff0000, v22
	global_store_dwordx2 v[26:27], v[2:3], off
	v_mov_b64_e32 v[10:11], v[200:201]
	v_mov_b64_e32 v[12:13], v[202:203]
	v_mov_b64_e32 v[18:19], v[204:205]
	v_mov_b64_e32 v[20:21], v[206:207]
	v_lshlrev_b32_e32 v28, 16, v23
	v_and_b32_e32 v23, 0xffff0000, v23
	v_lshlrev_b32_e32 v29, 16, v24
	v_and_b32_e32 v24, 0xffff0000, v24
	v_mul_f32_e32 v4, v5, v4
	v_mul_f32_e32 v22, v5, v22
	v_mul_f32_e32 v28, v5, v28
	v_mul_f32_e32 v23, v5, v23
	v_mul_f32_e32 v29, v5, v29
	v_mul_f32_e32 v24, v5, v24
	v_mov_b32_e32 v2, v37
	v_mov_b32_e32 v3, v37
	v_lshlrev_b32_e32 v30, 16, v25
	v_and_b32_e32 v25, 0xffff0000, v25
	v_mul_f32_e32 v30, v5, v30
	v_mul_f32_e32 v25, v5, v25
	v_mul_f32_e32 v4, v4, v10
	v_mul_f32_e32 v10, v22, v11
	v_mul_f32_e32 v11, v28, v12
	v_mul_f32_e32 v12, v23, v13
	v_mul_f32_e32 v13, v29, v18
	v_mul_f32_e32 v18, v24, v19
	v_cvt_pk_fp8_f32 v2, v4, v10
	v_cvt_pk_fp8_f32 v3, v13, v18
	v_mul_f32_e32 v4, v30, v20
	v_mul_f32_e32 v10, v25, v21
	v_cvt_pk_fp8_f32 v2, v11, v12 op_sel:[0,0,1]
	v_cvt_pk_fp8_f32 v3, v4, v10 op_sel:[0,0,1]
	s_waitcnt vmcnt(6)
	v_lshlrev_b32_e32 v4, 16, v14
	v_and_b32_e32 v14, 0xffff0000, v14
	v_lshlrev_b32_e32 v22, 16, v15
	global_store_dwordx2 v[26:27], v[2:3], off offset:512
	v_mov_b64_e32 v[10:11], v[208:209]
	v_mov_b64_e32 v[12:13], v[210:211]
	v_mov_b64_e32 v[18:19], v[236:237]
	v_mov_b64_e32 v[20:21], v[238:239]
	v_and_b32_e32 v15, 0xffff0000, v15
	v_lshlrev_b32_e32 v23, 16, v16
	v_and_b32_e32 v16, 0xffff0000, v16
	v_mul_f32_e32 v4, v5, v4
	v_mul_f32_e32 v14, v5, v14
	v_mul_f32_e32 v22, v5, v22
	v_mul_f32_e32 v15, v5, v15
	v_mul_f32_e32 v23, v5, v23
	v_mul_f32_e32 v16, v5, v16
	v_mov_b32_e32 v2, v37
	v_mov_b32_e32 v3, v37
	v_lshlrev_b32_e32 v24, 16, v17
	v_and_b32_e32 v17, 0xffff0000, v17
	v_mul_f32_e32 v24, v5, v24
	v_mul_f32_e32 v17, v5, v17
	v_mul_f32_e32 v4, v4, v10
	v_mul_f32_e32 v10, v14, v11
	v_mul_f32_e32 v11, v22, v12
	v_mul_f32_e32 v12, v15, v13
	v_mul_f32_e32 v13, v23, v18
	v_mul_f32_e32 v14, v16, v19
	v_cvt_pk_fp8_f32 v2, v4, v10
	v_cvt_pk_fp8_f32 v3, v13, v14
	v_mul_f32_e32 v4, v24, v20
	v_mul_f32_e32 v10, v17, v21
	v_cvt_pk_fp8_f32 v2, v11, v12 op_sel:[0,0,1]
	v_cvt_pk_fp8_f32 v3, v4, v10 op_sel:[0,0,1]
	s_waitcnt vmcnt(6)
	v_lshlrev_b32_e32 v4, 16, v6
	v_and_b32_e32 v6, 0xffff0000, v6
	v_lshlrev_b32_e32 v19, 16, v8
	global_store_dwordx2 v[26:27], v[2:3], off offset:1024
	v_mov_b64_e32 v[10:11], v[240:241]
	v_mov_b64_e32 v[12:13], v[242:243]
	v_mov_b64_e32 v[14:15], v[244:245]
	v_mov_b64_e32 v[16:17], v[246:247]
	v_and_b32_e32 v8, 0xffff0000, v8
	v_mul_f32_e32 v4, v5, v4
	v_mul_f32_e32 v6, v5, v6
	v_mul_f32_e32 v19, v5, v19
	v_mul_f32_e32 v8, v5, v8
	v_mov_b32_e32 v2, v37
	v_mov_b32_e32 v3, v37
	v_lshlrev_b32_e32 v18, 16, v7
	v_and_b32_e32 v7, 0xffff0000, v7
	v_lshlrev_b32_e32 v20, 16, v9
	v_and_b32_e32 v9, 0xffff0000, v9
	v_mul_f32_e32 v18, v5, v18
	v_mul_f32_e32 v7, v5, v7
	v_mul_f32_e32 v20, v5, v20
	v_mul_f32_e32 v5, v5, v9
	v_mul_f32_e32 v4, v4, v10
	v_mul_f32_e32 v6, v6, v11
	v_mul_f32_e32 v10, v19, v14
	v_mul_f32_e32 v8, v8, v15
	v_cvt_pk_fp8_f32 v2, v4, v6
	v_cvt_pk_fp8_f32 v3, v10, v8
	v_mul_f32_e32 v9, v18, v12
	v_mul_f32_e32 v7, v7, v13
	v_mul_f32_e32 v4, v20, v16
	v_mul_f32_e32 v5, v5, v17
	v_cvt_pk_fp8_f32 v2, v9, v7 op_sel:[0,0,1]
	v_cvt_pk_fp8_f32 v3, v4, v5 op_sel:[0,0,1]
	global_store_dwordx2 v[26:27], v[2:3], off offset:1536

.Lrt_tail:
	s_waitcnt vmcnt(0)
	v_lshlrev_b32_e32 v22, 16, v156
	v_and_b32_e32 v23, 0xffff0000, v156
	v_lshlrev_b32_e32 v26, 16, v157
	v_mfma_f32_32x32x2_f32 v[2:17], v22, v164, v[2:17]
	v_and_b32_e32 v27, 0xffff0000, v157
	v_mfma_f32_32x32x2_f32 v[2:17], v23, v165, v[2:17]
	v_lshlrev_b32_e32 v22, 16, v158
	v_mfma_f32_32x32x2_f32 v[2:17], v26, v166, v[2:17]
	v_and_b32_e32 v23, 0xffff0000, v158
	v_mfma_f32_32x32x2_f32 v[2:17], v27, v167, v[2:17]
	v_lshlrev_b32_e32 v26, 16, v159
	v_mfma_f32_32x32x2_f32 v[2:17], v22, v168, v[2:17]
	v_and_b32_e32 v27, 0xffff0000, v159
	v_mfma_f32_32x32x2_f32 v[2:17], v23, v169, v[2:17]
	v_lshlrev_b32_e32 v22, 16, v160
	v_mfma_f32_32x32x2_f32 v[2:17], v26, v170, v[2:17]
	v_and_b32_e32 v23, 0xffff0000, v160
	v_mfma_f32_32x32x2_f32 v[2:17], v27, v171, v[2:17]
	v_lshlrev_b32_e32 v26, 16, v161
	v_mfma_f32_32x32x2_f32 v[2:17], v22, v172, v[2:17]
	v_and_b32_e32 v27, 0xffff0000, v161
	v_mfma_f32_32x32x2_f32 v[2:17], v23, v173, v[2:17]
	v_lshlrev_b32_e32 v22, 16, v162
	v_mfma_f32_32x32x2_f32 v[2:17], v26, v174, v[2:17]
	v_and_b32_e32 v23, 0xffff0000, v162
	v_mfma_f32_32x32x2_f32 v[2:17], v27, v175, v[2:17]
	v_lshlrev_b32_e32 v26, 16, v163
	v_mfma_f32_32x32x2_f32 v[2:17], v22, v176, v[2:17]
	v_and_b32_e32 v27, 0xffff0000, v163
	v_mfma_f32_32x32x2_f32 v[2:17], v23, v177, v[2:17]
	v_mfma_f32_32x32x2_f32 v[2:17], v26, v178, v[2:17]
	v_mfma_f32_32x32x2_f32 v[2:17], v27, v179, v[2:17]
	v_lshl_or_b32 v18, s2, 6, v66
	v_or_b32_e32 v18, s3, v18
	s_movk_i32 s2, 0x84
	v_mad_u64_u32 v[18:19], s[2:3], v18, s2, v[34:35]
	s_nop 12
	ds_write2_b32 v18, v2, v3 offset0:64 offset1:97
	ds_write2_b32 v18, v4, v5 offset0:130 offset1:163
	v_add_u32_e32 v2, 0x400, v18
	ds_write2_b32 v2, v6, v7 offset0:72 offset1:105
	ds_write2_b32 v2, v8, v9 offset0:138 offset1:171
	v_add_u32_e32 v2, 0x800, v18
	ds_write2_b32 v2, v10, v11 offset0:80 offset1:113
	ds_write2_b32 v2, v12, v13 offset0:146 offset1:179
	v_add_u32_e32 v2, 0xc00, v18
	ds_write2_b32 v2, v14, v15 offset0:88 offset1:121
	ds_write2_b32 v2, v16, v17 offset0:154 offset1:187
	s_mov_b64 s[2:3], 0
	v_mov_b32_e32 v2, v70
	v_mov_b32_e32 v3, v69
	v_mov_b32_e32 v4, v68
	s_waitcnt lgkmcnt(0)
	s_barrier
	global_load_dword v182, v[50:51], off
.LBB0_994:
	ds_read_b32 v12, v2
	ds_read2st64_b32 v[6:7], v3 offset1:33
	ds_read2st64_b32 v[8:9], v3 offset0:66 offset1:99
	v_add_u32_e32 v4, 0x200, v4
	s_movk_i32 s12, 0x5ff
	v_cmp_lt_u32_e32 vcc, s12, v4
	s_waitcnt lgkmcnt(0)
	v_mov_b32_e32 v10, v6
	v_mov_b32_e32 v11, v8
	v_mov_b32_e32 v8, v7
	v_pk_add_f32 v[6:7], v[10:11], v[8:9]
	v_add_u32_e32 v2, 64, v2
	v_add_f32_e32 v6, v6, v7
	s_or_b64 s[2:3], vcc, s[2:3]
	s_waitcnt vmcnt(0)
	v_mov_b32_e32 v5, v182
	v_fmac_f32_e32 v5, v12, v6
	ds_write_b32 v3, v5 offset:33792
	v_add_u32_e32 v3, 0x840, v3
	s_andn2_b64 exec, exec, s[2:3]
	s_cbranch_execnz .LBB0_994
	s_or_b64 exec, exec, s[2:3]
	v_mov_b32_e32 v2, 0
	v_mov_b32_e32 v6, 0
	v_mov_b32_e32 v7, 0
	v_mov_b32_e32 v8, 0
	v_mov_b32_e32 v9, 0
	v_mov_b32_e32 v3, 0
	v_mov_b32_e32 v4, 0
	v_mov_b32_e32 v5, 0
	v_mov_b32_e32 v10, 0
	v_mov_b32_e32 v11, 0
	v_mov_b32_e32 v12, 0
	v_mov_b32_e32 v13, 0
	s_waitcnt lgkmcnt(0)
	s_barrier
	s_mov_b64 s[92:93], exec
	v_readlane_b32 s2, v252, 8
	v_readlane_b32 s3, v252, 9
	s_and_b64 s[2:3], s[92:93], s[2:3]
	s_mov_b64 exec, s[2:3]
	s_cbranch_execz .LBB0_997
	v_add_u32_e32 v2, 0x8500, v73
	ds_read2_b32 v[12:13], v2 offset1:1
	v_add_u32_e32 v2, 0x8508, v73
	v_add_u32_e32 v3, 0x8510, v73
	v_add_u32_e32 v4, 0x8518, v73
	ds_read2_b32 v[26:27], v2 offset1:1
	ds_read2_b32 v[16:17], v3 offset1:1
	ds_read2_b32 v[8:9], v4 offset1:1
	s_waitcnt lgkmcnt(3)
	v_max_f32_e32 v2, v12, v12
	v_max_f32_e32 v2, 0xff61b1e6, v2
	v_cmp_gt_f32_e32 vcc, v13, v2
	v_add_u32_e32 v4, 0x8520, v73
	ds_read2_b32 v[18:19], v4 offset1:1
	v_cndmask_b32_e32 v2, v2, v13, vcc
	v_cndmask_b32_e64 v3, 0, 1, vcc
	s_waitcnt lgkmcnt(3)
	v_cmp_gt_f32_e32 vcc, v26, v2
	v_add_u32_e32 v4, 0x8528, v73
	v_add_u32_e32 v5, 0x8530, v73
	v_cndmask_b32_e32 v2, v2, v26, vcc
	v_cndmask_b32_e64 v3, v3, 2, vcc
	v_cmp_gt_f32_e32 vcc, v27, v2
	v_add_u32_e32 v6, 0x8538, v73
	ds_read2_b32 v[32:33], v4 offset1:1
	ds_read2_b32 v[20:21], v5 offset1:1
	ds_read2_b32 v[10:11], v6 offset1:1
	v_cndmask_b32_e32 v2, v2, v27, vcc
	v_cndmask_b32_e64 v3, v3, 3, vcc
	s_waitcnt lgkmcnt(5)
	v_cmp_gt_f32_e32 vcc, v16, v2
	v_add_u32_e32 v4, 0x8540, v73
	ds_read2_b32 v[22:23], v4 offset1:1
	v_cndmask_b32_e32 v2, v2, v16, vcc
	v_cndmask_b32_e64 v3, v3, 4, vcc
	v_cmp_gt_f32_e32 vcc, v17, v2
	v_add_u32_e32 v4, 0x8548, v73
	v_add_u32_e32 v5, 0x8550, v73
	v_cndmask_b32_e32 v2, v2, v17, vcc
	v_cndmask_b32_e64 v3, v3, 5, vcc
	s_waitcnt lgkmcnt(5)
	v_cmp_gt_f32_e32 vcc, v8, v2
	v_add_u32_e32 v6, 0x8558, v73
	ds_read2_b32 v[58:59], v4 offset1:1
	ds_read2_b32 v[24:25], v5 offset1:1
	ds_read2_b32 v[14:15], v6 offset1:1
	v_cndmask_b32_e32 v2, v2, v8, vcc
	v_cndmask_b32_e64 v3, v3, 6, vcc
	v_cmp_gt_f32_e32 vcc, v9, v2
	v_add_u32_e32 v4, 0x8560, v73
	ds_read2_b32 v[28:29], v4 offset1:1
	v_cndmask_b32_e32 v2, v2, v9, vcc
	v_cndmask_b32_e64 v3, v3, 7, vcc
	s_waitcnt lgkmcnt(8)
	v_cmp_gt_f32_e32 vcc, v18, v2
	v_add_u32_e32 v4, 0x8568, v73
	v_add_u32_e32 v6, 0x8578, v73
	v_cndmask_b32_e32 v2, v2, v18, vcc
	v_cndmask_b32_e64 v3, v3, 8, vcc
	v_cmp_gt_f32_e32 vcc, v19, v2
	v_add_u32_e32 v5, 0x8570, v73
	ds_read2_b32 v[60:61], v4 offset1:1
	ds_read2_b32 v[30:31], v5 offset1:1
	ds_read2_b32 v[6:7], v6 offset1:1
	v_cndmask_b32_e32 v2, v2, v19, vcc
	v_cndmask_b32_e64 v3, v3, 9, vcc
	s_waitcnt lgkmcnt(10)
	v_cmp_gt_f32_e32 vcc, v32, v2
	s_mov_b32 s2, 0xff61b1e6
	v_cmp_lt_f32_e64 s[12:13], s2, v12
	v_cndmask_b32_e32 v2, v2, v32, vcc
	v_cndmask_b32_e64 v3, v3, 10, vcc
	v_cmp_gt_f32_e32 vcc, v33, v2
	s_nop 1
	v_cndmask_b32_e32 v2, v2, v33, vcc
	v_cndmask_b32_e64 v3, v3, 11, vcc
	s_waitcnt lgkmcnt(9)
	v_cmp_gt_f32_e32 vcc, v20, v2
	s_nop 1
	v_cndmask_b32_e32 v2, v2, v20, vcc
	v_cndmask_b32_e64 v3, v3, 12, vcc
	v_cmp_gt_f32_e32 vcc, v21, v2
	s_nop 1
	v_cndmask_b32_e32 v2, v2, v21, vcc
	v_cndmask_b32_e64 v3, v3, 13, vcc
	s_waitcnt lgkmcnt(8)
	v_cmp_gt_f32_e32 vcc, v10, v2
	s_nop 1
	v_cndmask_b32_e32 v2, v2, v10, vcc
	v_cndmask_b32_e64 v3, v3, 14, vcc
	v_cmp_gt_f32_e32 vcc, v11, v2
	s_nop 1
	v_cndmask_b32_e32 v2, v2, v11, vcc
	v_cndmask_b32_e64 v3, v3, 15, vcc
	s_waitcnt lgkmcnt(7)
	v_cmp_gt_f32_e32 vcc, v22, v2
	s_nop 1
	v_cndmask_b32_e32 v2, v2, v22, vcc
	v_cndmask_b32_e64 v3, v3, 16, vcc
	v_cmp_gt_f32_e32 vcc, v23, v2
	s_nop 1
	v_cndmask_b32_e32 v2, v2, v23, vcc
	v_cndmask_b32_e64 v3, v3, 17, vcc
	s_waitcnt lgkmcnt(6)
	v_cmp_gt_f32_e32 vcc, v58, v2
	s_nop 1
	v_cndmask_b32_e32 v2, v2, v58, vcc
	v_cndmask_b32_e64 v3, v3, 18, vcc
	v_cmp_gt_f32_e32 vcc, v59, v2
	s_nop 1
	v_cndmask_b32_e32 v2, v2, v59, vcc
	v_cndmask_b32_e64 v3, v3, 19, vcc
	s_waitcnt lgkmcnt(5)
	v_cmp_gt_f32_e32 vcc, v24, v2
	s_nop 1
	v_cndmask_b32_e32 v2, v2, v24, vcc
	v_cndmask_b32_e64 v3, v3, 20, vcc
	v_cmp_gt_f32_e32 vcc, v25, v2
	s_nop 1
	v_cndmask_b32_e32 v2, v2, v25, vcc
	v_cndmask_b32_e64 v3, v3, 21, vcc
	s_waitcnt lgkmcnt(4)
	v_cmp_gt_f32_e32 vcc, v14, v2
	s_nop 1
	v_cndmask_b32_e32 v2, v2, v14, vcc
	v_cndmask_b32_e64 v3, v3, 22, vcc
	v_cmp_gt_f32_e32 vcc, v15, v2
	s_nop 1
	v_cndmask_b32_e32 v2, v2, v15, vcc
	v_cndmask_b32_e64 v3, v3, 23, vcc
	s_waitcnt lgkmcnt(3)
	v_cmp_gt_f32_e32 vcc, v28, v2
	s_nop 1
	v_cndmask_b32_e32 v2, v2, v28, vcc
	v_cndmask_b32_e64 v3, v3, 24, vcc
	v_cmp_gt_f32_e32 vcc, v29, v2
	s_nop 1
	v_cndmask_b32_e32 v2, v2, v29, vcc
	v_cndmask_b32_e64 v3, v3, 25, vcc
	s_waitcnt lgkmcnt(2)
	v_cmp_gt_f32_e32 vcc, v60, v2
	s_nop 1
	v_cndmask_b32_e32 v2, v2, v60, vcc
	v_cndmask_b32_e64 v3, v3, 26, vcc
	v_cmp_gt_f32_e32 vcc, v61, v2
	s_nop 1
	v_cndmask_b32_e32 v2, v2, v61, vcc
	v_cndmask_b32_e64 v3, v3, 27, vcc
	s_waitcnt lgkmcnt(1)
	v_cmp_gt_f32_e32 vcc, v30, v2
	s_nop 1
	v_cndmask_b32_e32 v2, v2, v30, vcc
	v_cndmask_b32_e64 v3, v3, 28, vcc
	v_cmp_gt_f32_e32 vcc, v31, v2
	s_nop 1
	v_cndmask_b32_e32 v2, v2, v31, vcc
	v_cndmask_b32_e64 v3, v3, 29, vcc
	s_waitcnt lgkmcnt(0)
	v_cmp_gt_f32_e32 vcc, v6, v2
	s_nop 1
	v_cndmask_b32_e32 v5, v2, v6, vcc
	v_cndmask_b32_e64 v2, v3, 30, vcc
	v_cmp_gt_f32_e32 vcc, v7, v5
	s_nop 1
	v_cndmask_b32_e64 v2, v2, 31, vcc
	v_cmp_ne_u32_e64 s[14:15], 0, v2
	s_and_b64 s[14:15], s[14:15], s[12:13]
	v_cmp_ne_u32_e64 s[78:79], 1, v2
	v_cndmask_b32_e64 v3, v75, v12, s[14:15]
	v_cmp_gt_f32_e64 s[12:13], v13, v3
	s_and_b64 s[12:13], s[78:79], s[12:13]
	v_cmp_ne_u32_e64 s[76:77], 2, v2
	v_cndmask_b32_e64 v3, v3, v13, s[12:13]
	v_cndmask_b32_e64 v4, 0, 1, s[12:13]
	v_cmp_gt_f32_e64 s[12:13], v26, v3
	s_and_b64 s[12:13], s[76:77], s[12:13]
	v_cmp_ne_u32_e64 s[74:75], 3, v2
	v_cndmask_b32_e64 v3, v3, v26, s[12:13]
	v_cndmask_b32_e64 v4, v4, 2, s[12:13]
	v_cmp_gt_f32_e64 s[12:13], v27, v3
	s_and_b64 s[12:13], s[74:75], s[12:13]
	v_cmp_ne_u32_e64 s[72:73], 4, v2
	v_cndmask_b32_e64 v3, v3, v27, s[12:13]
	v_cndmask_b32_e64 v4, v4, 3, s[12:13]
	v_cmp_gt_f32_e64 s[12:13], v16, v3
	s_and_b64 s[12:13], s[72:73], s[12:13]
	v_cmp_ne_u32_e64 s[70:71], 5, v2
	v_cndmask_b32_e64 v3, v3, v16, s[12:13]
	v_cndmask_b32_e64 v4, v4, 4, s[12:13]
	v_cmp_gt_f32_e64 s[12:13], v17, v3
	s_and_b64 s[12:13], s[70:71], s[12:13]
	v_cmp_ne_u32_e64 s[68:69], 6, v2
	v_cndmask_b32_e64 v3, v3, v17, s[12:13]
	v_cndmask_b32_e64 v4, v4, 5, s[12:13]
	v_cmp_gt_f32_e64 s[12:13], v8, v3
	s_and_b64 s[12:13], s[68:69], s[12:13]
	v_cmp_ne_u32_e64 s[66:67], 7, v2
	v_cndmask_b32_e64 v3, v3, v8, s[12:13]
	v_cndmask_b32_e64 v4, v4, 6, s[12:13]
	v_cmp_gt_f32_e64 s[12:13], v9, v3
	s_and_b64 s[12:13], s[66:67], s[12:13]
	v_cmp_ne_u32_e64 s[64:65], 8, v2
	v_cndmask_b32_e64 v3, v3, v9, s[12:13]
	v_cndmask_b32_e64 v4, v4, 7, s[12:13]
	v_cmp_gt_f32_e64 s[12:13], v18, v3
	s_and_b64 s[12:13], s[64:65], s[12:13]
	v_cmp_ne_u32_e64 s[62:63], 9, v2
	v_cndmask_b32_e64 v3, v3, v18, s[12:13]
	v_cndmask_b32_e64 v4, v4, 8, s[12:13]
	v_cmp_gt_f32_e64 s[12:13], v19, v3
	s_and_b64 s[12:13], s[62:63], s[12:13]
	v_cmp_ne_u32_e64 s[60:61], 10, v2
	v_cndmask_b32_e64 v3, v3, v19, s[12:13]
	v_cndmask_b32_e64 v4, v4, 9, s[12:13]
	v_cmp_gt_f32_e64 s[12:13], v32, v3
	s_and_b64 s[12:13], s[60:61], s[12:13]
	v_cmp_ne_u32_e64 s[58:59], 11, v2
	v_cndmask_b32_e64 v3, v3, v32, s[12:13]
	v_cndmask_b32_e64 v4, v4, 10, s[12:13]
	v_cmp_gt_f32_e64 s[12:13], v33, v3
	s_and_b64 s[12:13], s[58:59], s[12:13]
	v_cmp_ne_u32_e64 s[56:57], 12, v2
	v_cndmask_b32_e64 v3, v3, v33, s[12:13]
	v_cndmask_b32_e64 v4, v4, 11, s[12:13]
	v_cmp_gt_f32_e64 s[12:13], v20, v3
	s_and_b64 s[12:13], s[56:57], s[12:13]
	v_cmp_ne_u32_e64 s[54:55], 13, v2
	v_cndmask_b32_e64 v3, v3, v20, s[12:13]
	v_cndmask_b32_e64 v4, v4, 12, s[12:13]
	v_cmp_gt_f32_e64 s[12:13], v21, v3
	s_and_b64 s[12:13], s[54:55], s[12:13]
	v_cmp_ne_u32_e64 s[52:53], 14, v2
	v_cndmask_b32_e64 v3, v3, v21, s[12:13]
	v_cndmask_b32_e64 v4, v4, 13, s[12:13]
	v_cmp_gt_f32_e64 s[12:13], v10, v3
	s_and_b64 s[12:13], s[52:53], s[12:13]
	v_cmp_ne_u32_e64 s[50:51], 15, v2
	v_cndmask_b32_e64 v3, v3, v10, s[12:13]
	v_cndmask_b32_e64 v4, v4, 14, s[12:13]
	v_cmp_gt_f32_e64 s[12:13], v11, v3
	s_and_b64 s[12:13], s[50:51], s[12:13]
	v_cmp_ne_u32_e64 s[48:49], 16, v2
	v_cndmask_b32_e64 v3, v3, v11, s[12:13]
	v_cndmask_b32_e64 v4, v4, 15, s[12:13]
	v_cmp_gt_f32_e64 s[12:13], v22, v3
	s_and_b64 s[12:13], s[48:49], s[12:13]
	v_cmp_ne_u32_e64 s[46:47], 17, v2
	v_cndmask_b32_e64 v3, v3, v22, s[12:13]
	v_cndmask_b32_e64 v4, v4, 16, s[12:13]
	v_cmp_gt_f32_e64 s[12:13], v23, v3
	s_and_b64 s[12:13], s[46:47], s[12:13]
	v_cmp_ne_u32_e64 s[44:45], 18, v2
	v_cndmask_b32_e64 v3, v3, v23, s[12:13]
	v_cndmask_b32_e64 v4, v4, 17, s[12:13]
	v_cmp_gt_f32_e64 s[12:13], v58, v3
	s_and_b64 s[12:13], s[44:45], s[12:13]
	v_cmp_ne_u32_e64 s[42:43], 19, v2
	v_cndmask_b32_e64 v3, v3, v58, s[12:13]
	v_cndmask_b32_e64 v4, v4, 18, s[12:13]
	v_cmp_gt_f32_e64 s[12:13], v59, v3
	s_and_b64 s[12:13], s[42:43], s[12:13]
	v_cmp_ne_u32_e64 s[40:41], 20, v2
	v_cndmask_b32_e64 v3, v3, v59, s[12:13]
	v_cndmask_b32_e64 v4, v4, 19, s[12:13]
	v_cmp_gt_f32_e64 s[12:13], v24, v3
	s_and_b64 s[12:13], s[40:41], s[12:13]
	v_cmp_ne_u32_e64 s[38:39], 21, v2
	v_cndmask_b32_e64 v3, v3, v24, s[12:13]
	v_cndmask_b32_e64 v4, v4, 20, s[12:13]
	v_cmp_gt_f32_e64 s[12:13], v25, v3
	s_and_b64 s[12:13], s[38:39], s[12:13]
	v_cmp_ne_u32_e64 s[36:37], 22, v2
	v_cndmask_b32_e64 v3, v3, v25, s[12:13]
	v_cndmask_b32_e64 v4, v4, 21, s[12:13]
	v_cmp_gt_f32_e64 s[12:13], v14, v3
	s_and_b64 s[12:13], s[36:37], s[12:13]
	v_cmp_ne_u32_e64 s[34:35], 23, v2
	v_cndmask_b32_e64 v3, v3, v14, s[12:13]
	v_cndmask_b32_e64 v4, v4, 22, s[12:13]
	v_cmp_gt_f32_e64 s[12:13], v15, v3
	s_and_b64 s[12:13], s[34:35], s[12:13]
	v_cmp_ne_u32_e64 s[30:31], 24, v2
	v_cndmask_b32_e64 v3, v3, v15, s[12:13]
	v_cndmask_b32_e64 v4, v4, 23, s[12:13]
	v_cmp_gt_f32_e64 s[12:13], v28, v3
	s_and_b64 s[12:13], s[30:31], s[12:13]
	v_cmp_ne_u32_e64 s[28:29], 25, v2
	v_cndmask_b32_e64 v3, v3, v28, s[12:13]
	v_cndmask_b32_e64 v4, v4, 24, s[12:13]
	v_cmp_gt_f32_e64 s[12:13], v29, v3
	s_and_b64 s[12:13], s[28:29], s[12:13]
	v_cmp_ne_u32_e64 s[26:27], 26, v2
	v_cndmask_b32_e64 v3, v3, v29, s[12:13]
	v_cndmask_b32_e64 v4, v4, 25, s[12:13]
	v_cmp_gt_f32_e64 s[12:13], v60, v3
	s_and_b64 s[12:13], s[26:27], s[12:13]
	v_cmp_ne_u32_e64 s[24:25], 27, v2
	v_cndmask_b32_e64 v3, v3, v60, s[12:13]
	v_cndmask_b32_e64 v4, v4, 26, s[12:13]
	v_cmp_gt_f32_e64 s[12:13], v61, v3
	s_and_b64 s[12:13], s[24:25], s[12:13]
	v_cmp_ne_u32_e64 s[22:23], 28, v2
	v_cndmask_b32_e64 v3, v3, v61, s[12:13]
	v_cndmask_b32_e64 v4, v4, 27, s[12:13]
	v_cmp_gt_f32_e64 s[12:13], v30, v3
	s_and_b64 s[12:13], s[22:23], s[12:13]
	v_cmp_ne_u32_e64 s[20:21], 29, v2
	v_cndmask_b32_e64 v3, v3, v30, s[12:13]
	v_cndmask_b32_e64 v4, v4, 28, s[12:13]
	v_cmp_gt_f32_e64 s[12:13], v31, v3
	s_and_b64 s[12:13], s[20:21], s[12:13]
	v_cmp_ne_u32_e64 s[18:19], 30, v2
	v_cndmask_b32_e64 v3, v3, v31, s[12:13]
	v_cndmask_b32_e64 v4, v4, 29, s[12:13]
	v_cmp_gt_f32_e64 s[12:13], v6, v3
	s_and_b64 s[12:13], s[18:19], s[12:13]
	v_cmp_ne_u32_e64 s[16:17], 31, v2
	v_cndmask_b32_e64 v36, v3, v6, s[12:13]
	v_cndmask_b32_e64 v3, v4, 30, s[12:13]
	v_cmp_gt_f32_e64 s[12:13], v7, v36
	s_and_b64 s[12:13], s[16:17], s[12:13]
	v_cndmask_b32_e32 v5, v5, v7, vcc
	v_cndmask_b32_e64 v3, v3, 31, s[12:13]
	v_cmp_ne_u32_e64 s[80:81], 0, v3
	s_and_b64 s[14:15], s[14:15], s[80:81]
	v_cndmask_b32_e64 v4, v75, v12, s[14:15]
	v_cmp_ne_u32_e64 s[80:81], 1, v3
	s_and_b64 s[80:81], s[78:79], s[80:81]
	v_cmp_gt_f32_e64 s[78:79], v13, v4
	s_and_b64 s[78:79], s[80:81], s[78:79]
	v_cndmask_b32_e64 v36, v36, v7, s[12:13]
	v_cndmask_b32_e64 v4, v4, v13, s[78:79]
	v_cndmask_b32_e64 v77, 0, 1, s[78:79]
	v_cmp_ne_u32_e64 s[78:79], 2, v3
	s_and_b64 s[78:79], s[76:77], s[78:79]
	v_cmp_gt_f32_e64 s[76:77], v26, v4
	s_and_b64 s[76:77], s[78:79], s[76:77]
	s_nop 0
	v_cndmask_b32_e64 v4, v4, v26, s[76:77]
	v_cndmask_b32_e64 v77, v77, 2, s[76:77]
	v_cmp_ne_u32_e64 s[76:77], 3, v3
	s_and_b64 s[76:77], s[74:75], s[76:77]
	v_cmp_gt_f32_e64 s[74:75], v27, v4
	s_and_b64 s[74:75], s[76:77], s[74:75]
	s_nop 0
	v_cndmask_b32_e64 v4, v4, v27, s[74:75]
	v_cndmask_b32_e64 v77, v77, 3, s[74:75]
	v_cmp_ne_u32_e64 s[74:75], 4, v3
	s_and_b64 s[74:75], s[72:73], s[74:75]
	v_cmp_gt_f32_e64 s[72:73], v16, v4
	s_and_b64 s[72:73], s[74:75], s[72:73]
	s_nop 0
	v_cndmask_b32_e64 v4, v4, v16, s[72:73]
	v_cndmask_b32_e64 v77, v77, 4, s[72:73]
	v_cmp_ne_u32_e64 s[72:73], 5, v3
	s_and_b64 s[72:73], s[70:71], s[72:73]
	v_cmp_gt_f32_e64 s[70:71], v17, v4
	s_and_b64 s[70:71], s[72:73], s[70:71]
	s_nop 0
	v_cndmask_b32_e64 v4, v4, v17, s[70:71]
	v_cndmask_b32_e64 v77, v77, 5, s[70:71]
	v_cmp_ne_u32_e64 s[70:71], 6, v3
	s_and_b64 s[70:71], s[68:69], s[70:71]
	v_cmp_gt_f32_e64 s[68:69], v8, v4
	s_and_b64 s[68:69], s[70:71], s[68:69]
	s_nop 0
	v_cndmask_b32_e64 v4, v4, v8, s[68:69]
	v_cndmask_b32_e64 v77, v77, 6, s[68:69]
	v_cmp_ne_u32_e64 s[68:69], 7, v3
	s_and_b64 s[68:69], s[66:67], s[68:69]
	v_cmp_gt_f32_e64 s[66:67], v9, v4
	s_and_b64 s[66:67], s[68:69], s[66:67]
	s_nop 0
	v_cndmask_b32_e64 v4, v4, v9, s[66:67]
	v_cndmask_b32_e64 v77, v77, 7, s[66:67]
	v_cmp_ne_u32_e64 s[66:67], 8, v3
	s_and_b64 s[66:67], s[64:65], s[66:67]
	v_cmp_gt_f32_e64 s[64:65], v18, v4
	s_and_b64 s[64:65], s[66:67], s[64:65]
	s_nop 0
	v_cndmask_b32_e64 v4, v4, v18, s[64:65]
	v_cndmask_b32_e64 v77, v77, 8, s[64:65]
	v_cmp_ne_u32_e64 s[64:65], 9, v3
	s_and_b64 s[64:65], s[62:63], s[64:65]
	v_cmp_gt_f32_e64 s[62:63], v19, v4
	s_and_b64 s[62:63], s[64:65], s[62:63]
	s_nop 0
	v_cndmask_b32_e64 v4, v4, v19, s[62:63]
	v_cndmask_b32_e64 v77, v77, 9, s[62:63]
	v_cmp_ne_u32_e64 s[62:63], 10, v3
	s_and_b64 s[62:63], s[60:61], s[62:63]
	v_cmp_gt_f32_e64 s[60:61], v32, v4
	s_and_b64 s[60:61], s[62:63], s[60:61]
	s_nop 0
	v_cndmask_b32_e64 v4, v4, v32, s[60:61]
	v_cndmask_b32_e64 v77, v77, 10, s[60:61]
	v_cmp_ne_u32_e64 s[60:61], 11, v3
	s_and_b64 s[60:61], s[58:59], s[60:61]
	v_cmp_gt_f32_e64 s[58:59], v33, v4
	s_and_b64 s[58:59], s[60:61], s[58:59]
	s_nop 0
	v_cndmask_b32_e64 v4, v4, v33, s[58:59]
	v_cndmask_b32_e64 v77, v77, 11, s[58:59]
	v_cmp_ne_u32_e64 s[58:59], 12, v3
	s_and_b64 s[58:59], s[56:57], s[58:59]
	v_cmp_gt_f32_e64 s[56:57], v20, v4
	s_and_b64 s[56:57], s[58:59], s[56:57]
	s_nop 0
	v_cndmask_b32_e64 v4, v4, v20, s[56:57]
	v_cndmask_b32_e64 v77, v77, 12, s[56:57]
	v_cmp_ne_u32_e64 s[56:57], 13, v3
	s_and_b64 s[56:57], s[54:55], s[56:57]
	v_cmp_gt_f32_e64 s[54:55], v21, v4
	s_and_b64 s[54:55], s[56:57], s[54:55]
	s_nop 0
	v_cndmask_b32_e64 v4, v4, v21, s[54:55]
	v_cndmask_b32_e64 v77, v77, 13, s[54:55]
	v_cmp_ne_u32_e64 s[54:55], 14, v3
	s_and_b64 s[54:55], s[52:53], s[54:55]
	v_cmp_gt_f32_e64 s[52:53], v10, v4
	s_and_b64 s[52:53], s[54:55], s[52:53]
	s_nop 0
	v_cndmask_b32_e64 v4, v4, v10, s[52:53]
	v_cndmask_b32_e64 v77, v77, 14, s[52:53]
	v_cmp_ne_u32_e64 s[52:53], 15, v3
	s_and_b64 s[52:53], s[50:51], s[52:53]
	v_cmp_gt_f32_e64 s[50:51], v11, v4
	s_and_b64 s[50:51], s[52:53], s[50:51]
	s_nop 0
	v_cndmask_b32_e64 v4, v4, v11, s[50:51]
	v_cndmask_b32_e64 v77, v77, 15, s[50:51]
	v_cmp_ne_u32_e64 s[50:51], 16, v3
	s_and_b64 s[50:51], s[48:49], s[50:51]
	v_cmp_gt_f32_e64 s[48:49], v22, v4
	s_and_b64 s[48:49], s[50:51], s[48:49]
	s_nop 0
	v_cndmask_b32_e64 v4, v4, v22, s[48:49]
	v_cndmask_b32_e64 v77, v77, 16, s[48:49]
	v_cmp_ne_u32_e64 s[48:49], 17, v3
	s_and_b64 s[48:49], s[46:47], s[48:49]
	v_cmp_gt_f32_e64 s[46:47], v23, v4
	s_and_b64 s[46:47], s[48:49], s[46:47]
	s_nop 0
	v_cndmask_b32_e64 v4, v4, v23, s[46:47]
	v_cndmask_b32_e64 v77, v77, 17, s[46:47]
	v_cmp_ne_u32_e64 s[46:47], 18, v3
	s_and_b64 s[46:47], s[44:45], s[46:47]
	v_cmp_gt_f32_e64 s[44:45], v58, v4
	s_and_b64 s[44:45], s[46:47], s[44:45]
	s_nop 0
	v_cndmask_b32_e64 v4, v4, v58, s[44:45]
	v_cndmask_b32_e64 v77, v77, 18, s[44:45]
	v_cmp_ne_u32_e64 s[44:45], 19, v3
	s_and_b64 s[44:45], s[42:43], s[44:45]
	v_cmp_gt_f32_e64 s[42:43], v59, v4
	s_and_b64 s[42:43], s[44:45], s[42:43]
	s_nop 0
	v_cndmask_b32_e64 v4, v4, v59, s[42:43]
	v_cndmask_b32_e64 v77, v77, 19, s[42:43]
	v_cmp_ne_u32_e64 s[42:43], 20, v3
	s_and_b64 s[42:43], s[40:41], s[42:43]
	v_cmp_gt_f32_e64 s[40:41], v24, v4
	s_and_b64 s[40:41], s[42:43], s[40:41]
	s_nop 0
	v_cndmask_b32_e64 v4, v4, v24, s[40:41]
	v_cndmask_b32_e64 v77, v77, 20, s[40:41]
	v_cmp_ne_u32_e64 s[40:41], 21, v3
	s_and_b64 s[40:41], s[38:39], s[40:41]
	v_cmp_gt_f32_e64 s[38:39], v25, v4
	s_and_b64 s[38:39], s[40:41], s[38:39]
	s_nop 0
	v_cndmask_b32_e64 v4, v4, v25, s[38:39]
	v_cndmask_b32_e64 v77, v77, 21, s[38:39]
	v_cmp_ne_u32_e64 s[38:39], 22, v3
	s_and_b64 s[38:39], s[36:37], s[38:39]
	v_cmp_gt_f32_e64 s[36:37], v14, v4
	s_and_b64 s[36:37], s[38:39], s[36:37]
	s_nop 0
	v_cndmask_b32_e64 v4, v4, v14, s[36:37]
	v_cndmask_b32_e64 v77, v77, 22, s[36:37]
	v_cmp_ne_u32_e64 s[36:37], 23, v3
	s_and_b64 s[36:37], s[34:35], s[36:37]
	v_cmp_gt_f32_e64 s[34:35], v15, v4
	s_and_b64 s[34:35], s[36:37], s[34:35]
	s_nop 0
	v_cndmask_b32_e64 v4, v4, v15, s[34:35]
	v_cndmask_b32_e64 v77, v77, 23, s[34:35]
	v_cmp_ne_u32_e64 s[34:35], 24, v3
	s_and_b64 s[34:35], s[30:31], s[34:35]
	v_cmp_gt_f32_e64 s[30:31], v28, v4
	s_and_b64 s[30:31], s[34:35], s[30:31]
	s_nop 0
	v_cndmask_b32_e64 v4, v4, v28, s[30:31]
	v_cndmask_b32_e64 v77, v77, 24, s[30:31]
	v_cmp_ne_u32_e64 s[30:31], 25, v3
	s_and_b64 s[30:31], s[28:29], s[30:31]
	v_cmp_gt_f32_e64 s[28:29], v29, v4
	s_and_b64 s[28:29], s[30:31], s[28:29]
	s_nop 0
	v_cndmask_b32_e64 v4, v4, v29, s[28:29]
	v_cndmask_b32_e64 v77, v77, 25, s[28:29]
	v_cmp_ne_u32_e64 s[28:29], 26, v3
	s_and_b64 s[28:29], s[26:27], s[28:29]
	v_cmp_gt_f32_e64 s[26:27], v60, v4
	s_and_b64 s[26:27], s[28:29], s[26:27]
	s_nop 0
	v_cndmask_b32_e64 v4, v4, v60, s[26:27]
	v_cndmask_b32_e64 v77, v77, 26, s[26:27]
	v_cmp_ne_u32_e64 s[26:27], 27, v3
	s_and_b64 s[26:27], s[24:25], s[26:27]
	v_cmp_gt_f32_e64 s[24:25], v61, v4
	s_and_b64 s[24:25], s[26:27], s[24:25]
	s_nop 0
	v_cndmask_b32_e64 v4, v4, v61, s[24:25]
	v_cndmask_b32_e64 v77, v77, 27, s[24:25]
	v_cmp_ne_u32_e64 s[24:25], 28, v3
	s_and_b64 s[24:25], s[22:23], s[24:25]
	v_cmp_gt_f32_e64 s[22:23], v30, v4
	s_and_b64 s[22:23], s[24:25], s[22:23]
	s_nop 0
	v_cndmask_b32_e64 v4, v4, v30, s[22:23]
	v_cndmask_b32_e64 v77, v77, 28, s[22:23]
	v_cmp_ne_u32_e64 s[22:23], 29, v3
	s_and_b64 s[22:23], s[20:21], s[22:23]
	v_cmp_gt_f32_e64 s[20:21], v31, v4
	s_and_b64 s[20:21], s[22:23], s[20:21]
	s_nop 0
	v_cndmask_b32_e64 v4, v4, v31, s[20:21]
	v_cndmask_b32_e64 v77, v77, 29, s[20:21]
	v_cmp_ne_u32_e64 s[20:21], 30, v3
	s_and_b64 s[20:21], s[18:19], s[20:21]
	v_cmp_gt_f32_e64 s[18:19], v6, v4
	s_and_b64 s[18:19], s[20:21], s[18:19]
	s_nop 0
	v_cndmask_b32_e64 v78, v4, v6, s[18:19]
	v_cndmask_b32_e64 v4, v77, 30, s[18:19]
	v_cmp_ne_u32_e64 s[18:19], 31, v3
	s_and_b64 s[2:3], s[16:17], s[18:19]
	v_cmp_gt_f32_e64 s[16:17], v7, v78
	s_and_b64 s[12:13], s[2:3], s[16:17]
	v_cndmask_b32_e64 v4, v4, 31, s[12:13]
	v_cmp_ne_u32_e64 s[16:17], 0, v4
	s_and_b64 s[14:15], s[14:15], s[16:17]
	v_cndmask_b32_e64 v12, v75, v12, s[14:15]
	v_cmp_ne_u32_e64 s[14:15], 1, v4
	s_and_b64 s[16:17], s[80:81], s[14:15]
	v_cmp_gt_f32_e64 s[14:15], v13, v12
	s_and_b64 s[14:15], s[16:17], s[14:15]
	v_readlane_b32 s80, v252, 45
	v_cndmask_b32_e64 v12, v12, v13, s[14:15]
	v_cndmask_b32_e64 v13, 0, 1, s[14:15]
	v_cmp_ne_u32_e64 s[14:15], 2, v4
	s_and_b64 s[16:17], s[78:79], s[14:15]
	v_cmp_gt_f32_e64 s[14:15], v26, v12
	s_and_b64 s[14:15], s[16:17], s[14:15]
	v_readlane_b32 s81, v252, 46
	v_cndmask_b32_e64 v12, v12, v26, s[14:15]
	v_cndmask_b32_e64 v13, v13, 2, s[14:15]
	v_cmp_ne_u32_e64 s[14:15], 3, v4
	s_and_b64 s[16:17], s[76:77], s[14:15]
	v_cmp_gt_f32_e64 s[14:15], v27, v12
	s_and_b64 s[14:15], s[16:17], s[14:15]
	s_nop 0
	v_cndmask_b32_e64 v12, v12, v27, s[14:15]
	v_cndmask_b32_e64 v13, v13, 3, s[14:15]
	v_cmp_ne_u32_e64 s[14:15], 4, v4
	s_and_b64 s[16:17], s[74:75], s[14:15]
	v_cmp_gt_f32_e64 s[14:15], v16, v12
	s_and_b64 s[14:15], s[16:17], s[14:15]
	s_nop 0
	v_cndmask_b32_e64 v12, v12, v16, s[14:15]
	v_cndmask_b32_e64 v13, v13, 4, s[14:15]
	v_cmp_ne_u32_e64 s[14:15], 5, v4
	s_and_b64 s[16:17], s[72:73], s[14:15]
	v_cmp_gt_f32_e64 s[14:15], v17, v12
	s_and_b64 s[14:15], s[16:17], s[14:15]
	s_nop 0
	v_cndmask_b32_e64 v12, v12, v17, s[14:15]
	v_cndmask_b32_e64 v13, v13, 5, s[14:15]
	v_cmp_ne_u32_e64 s[14:15], 6, v4
	s_and_b64 s[16:17], s[70:71], s[14:15]
	v_cmp_gt_f32_e64 s[14:15], v8, v12
	s_and_b64 s[14:15], s[16:17], s[14:15]
	s_nop 0
	v_cndmask_b32_e64 v8, v12, v8, s[14:15]
	v_cndmask_b32_e64 v12, v13, 6, s[14:15]
	v_cmp_ne_u32_e64 s[14:15], 7, v4
	s_and_b64 s[16:17], s[68:69], s[14:15]
	v_cmp_gt_f32_e64 s[14:15], v9, v8
	s_and_b64 s[14:15], s[16:17], s[14:15]
	s_nop 0
	v_cndmask_b32_e64 v8, v8, v9, s[14:15]
	v_cndmask_b32_e64 v9, v12, 7, s[14:15]
	v_cmp_ne_u32_e64 s[14:15], 8, v4
	s_and_b64 s[16:17], s[66:67], s[14:15]
	v_cmp_gt_f32_e64 s[14:15], v18, v8
	s_and_b64 s[14:15], s[16:17], s[14:15]
	s_nop 0
	v_cndmask_b32_e64 v8, v8, v18, s[14:15]
	v_cndmask_b32_e64 v9, v9, 8, s[14:15]
	v_cmp_ne_u32_e64 s[14:15], 9, v4
	s_and_b64 s[16:17], s[64:65], s[14:15]
	v_cmp_gt_f32_e64 s[14:15], v19, v8
	s_and_b64 s[14:15], s[16:17], s[14:15]
	s_nop 0
	v_cndmask_b32_e64 v8, v8, v19, s[14:15]
	v_cndmask_b32_e64 v9, v9, 9, s[14:15]
	v_cmp_ne_u32_e64 s[14:15], 10, v4
	s_and_b64 s[16:17], s[62:63], s[14:15]
	v_cmp_gt_f32_e64 s[14:15], v32, v8
	s_and_b64 s[14:15], s[16:17], s[14:15]
	s_nop 0
	v_cndmask_b32_e64 v8, v8, v32, s[14:15]
	v_cndmask_b32_e64 v9, v9, 10, s[14:15]
	v_cmp_ne_u32_e64 s[14:15], 11, v4
	s_and_b64 s[16:17], s[60:61], s[14:15]
	v_cmp_gt_f32_e64 s[14:15], v33, v8
	s_and_b64 s[14:15], s[16:17], s[14:15]
	s_nop 0
	v_cndmask_b32_e64 v8, v8, v33, s[14:15]
	v_cndmask_b32_e64 v9, v9, 11, s[14:15]
	v_cmp_ne_u32_e64 s[14:15], 12, v4
	s_and_b64 s[16:17], s[58:59], s[14:15]
	v_cmp_gt_f32_e64 s[14:15], v20, v8
	s_and_b64 s[14:15], s[16:17], s[14:15]
	s_nop 0
	v_cndmask_b32_e64 v8, v8, v20, s[14:15]
	v_cndmask_b32_e64 v9, v9, 12, s[14:15]
	v_cmp_ne_u32_e64 s[14:15], 13, v4
	s_and_b64 s[16:17], s[56:57], s[14:15]
	v_cmp_gt_f32_e64 s[14:15], v21, v8
	s_and_b64 s[14:15], s[16:17], s[14:15]
	s_nop 0
	v_cndmask_b32_e64 v8, v8, v21, s[14:15]
	v_cndmask_b32_e64 v9, v9, 13, s[14:15]
	v_cmp_ne_u32_e64 s[14:15], 14, v4
	s_and_b64 s[16:17], s[54:55], s[14:15]
	v_cmp_gt_f32_e64 s[14:15], v10, v8
	s_and_b64 s[14:15], s[16:17], s[14:15]
	s_nop 0
	v_cndmask_b32_e64 v8, v8, v10, s[14:15]
	v_cndmask_b32_e64 v9, v9, 14, s[14:15]
	v_cmp_ne_u32_e64 s[14:15], 15, v4
	s_and_b64 s[16:17], s[52:53], s[14:15]
	v_cmp_gt_f32_e64 s[14:15], v11, v8
	s_and_b64 s[14:15], s[16:17], s[14:15]
	s_nop 0
	v_cndmask_b32_e64 v8, v8, v11, s[14:15]
	v_cndmask_b32_e64 v9, v9, 15, s[14:15]
	v_cmp_ne_u32_e64 s[14:15], 16, v4
	s_and_b64 s[16:17], s[50:51], s[14:15]
	v_cmp_gt_f32_e64 s[14:15], v22, v8
	s_and_b64 s[14:15], s[16:17], s[14:15]
	s_nop 0
	v_cndmask_b32_e64 v8, v8, v22, s[14:15]
	v_cndmask_b32_e64 v9, v9, 16, s[14:15]
	v_cmp_ne_u32_e64 s[14:15], 17, v4
	s_and_b64 s[16:17], s[48:49], s[14:15]
	v_cmp_gt_f32_e64 s[14:15], v23, v8
	s_and_b64 s[14:15], s[16:17], s[14:15]
	s_nop 0
	v_cndmask_b32_e64 v8, v8, v23, s[14:15]
	v_cndmask_b32_e64 v9, v9, 17, s[14:15]
	v_cmp_ne_u32_e64 s[14:15], 18, v4
	s_and_b64 s[16:17], s[46:47], s[14:15]
	v_cmp_gt_f32_e64 s[14:15], v58, v8
	s_and_b64 s[14:15], s[16:17], s[14:15]
	s_nop 0
	v_cndmask_b32_e64 v8, v8, v58, s[14:15]
	v_cndmask_b32_e64 v9, v9, 18, s[14:15]
	v_cmp_ne_u32_e64 s[14:15], 19, v4
	s_and_b64 s[16:17], s[44:45], s[14:15]
	v_cmp_gt_f32_e64 s[14:15], v59, v8
	s_and_b64 s[14:15], s[16:17], s[14:15]
	s_nop 0
	v_cndmask_b32_e64 v8, v8, v59, s[14:15]
	v_cndmask_b32_e64 v9, v9, 19, s[14:15]
	v_cmp_ne_u32_e64 s[14:15], 20, v4
	s_and_b64 s[16:17], s[42:43], s[14:15]
	v_cmp_gt_f32_e64 s[14:15], v24, v8
	s_and_b64 s[14:15], s[16:17], s[14:15]
	s_nop 0
	v_cndmask_b32_e64 v8, v8, v24, s[14:15]
	v_cndmask_b32_e64 v9, v9, 20, s[14:15]
	v_cmp_ne_u32_e64 s[14:15], 21, v4
	s_and_b64 s[16:17], s[40:41], s[14:15]
	v_cmp_gt_f32_e64 s[14:15], v25, v8
	s_and_b64 s[14:15], s[16:17], s[14:15]
	s_nop 0
	v_cndmask_b32_e64 v8, v8, v25, s[14:15]
	v_cndmask_b32_e64 v9, v9, 21, s[14:15]
	v_cmp_ne_u32_e64 s[14:15], 22, v4
	s_and_b64 s[16:17], s[38:39], s[14:15]
	v_cmp_gt_f32_e64 s[14:15], v14, v8
	s_and_b64 s[14:15], s[16:17], s[14:15]
	s_nop 0
	v_cndmask_b32_e64 v8, v8, v14, s[14:15]
	v_cndmask_b32_e64 v9, v9, 22, s[14:15]
	v_cmp_ne_u32_e64 s[14:15], 23, v4
	s_and_b64 s[16:17], s[36:37], s[14:15]
	v_cmp_gt_f32_e64 s[14:15], v15, v8
	s_and_b64 s[14:15], s[16:17], s[14:15]
	s_nop 0
	v_cndmask_b32_e64 v8, v8, v15, s[14:15]
	v_cndmask_b32_e64 v9, v9, 23, s[14:15]
	v_cmp_ne_u32_e64 s[14:15], 24, v4
	s_and_b64 s[16:17], s[34:35], s[14:15]
	v_cmp_gt_f32_e64 s[14:15], v28, v8
	s_and_b64 s[14:15], s[16:17], s[14:15]
	s_nop 0
	v_cndmask_b32_e64 v8, v8, v28, s[14:15]
	v_cndmask_b32_e64 v9, v9, 24, s[14:15]
	v_cmp_ne_u32_e64 s[14:15], 25, v4
	s_and_b64 s[16:17], s[30:31], s[14:15]
	v_cmp_gt_f32_e64 s[14:15], v29, v8
	s_and_b64 s[14:15], s[16:17], s[14:15]
	s_nop 0
	v_cndmask_b32_e64 v8, v8, v29, s[14:15]
	v_cndmask_b32_e64 v9, v9, 25, s[14:15]
	v_cmp_ne_u32_e64 s[14:15], 26, v4
	s_and_b64 s[16:17], s[28:29], s[14:15]
	v_cmp_gt_f32_e64 s[14:15], v60, v8
	s_and_b64 s[14:15], s[16:17], s[14:15]
	s_nop 0
	v_cndmask_b32_e64 v8, v8, v60, s[14:15]
	v_cndmask_b32_e64 v9, v9, 26, s[14:15]
	v_cmp_ne_u32_e64 s[14:15], 27, v4
	s_and_b64 s[16:17], s[26:27], s[14:15]
	v_cmp_gt_f32_e64 s[14:15], v61, v8
	s_and_b64 s[14:15], s[16:17], s[14:15]
	s_nop 0
	v_cndmask_b32_e64 v8, v8, v61, s[14:15]
	v_cndmask_b32_e64 v9, v9, 27, s[14:15]
	v_cmp_ne_u32_e64 s[14:15], 28, v4
	s_and_b64 s[16:17], s[24:25], s[14:15]
	v_cmp_gt_f32_e64 s[14:15], v30, v8
	s_and_b64 s[14:15], s[16:17], s[14:15]
	s_nop 0
	v_cndmask_b32_e64 v8, v8, v30, s[14:15]
	v_cndmask_b32_e64 v10, v9, 28, s[14:15]
	v_cmp_ne_u32_e64 s[14:15], 29, v4
	s_and_b64 s[16:17], s[22:23], s[14:15]
	v_cmp_gt_f32_e64 s[14:15], v31, v8
	s_and_b64 s[14:15], s[16:17], s[14:15]
	v_cmp_ne_u32_e64 s[16:17], 30, v4
	v_cndmask_b32_e64 v8, v8, v31, s[14:15]
	s_and_b64 s[18:19], s[20:21], s[16:17]
	v_cmp_gt_f32_e64 s[16:17], v6, v8
	s_and_b64 s[16:17], s[18:19], s[16:17]
	v_cmp_ne_u32_e64 s[18:19], 31, v4
	v_cndmask_b32_e64 v6, v8, v6, s[16:17]
	v_sub_f32_e32 v8, v36, v5
	v_mul_f32_e32 v9, 0x3fb8aa3b, v8
	v_fma_f32 v11, v8, s89, -v9
	v_rndne_f32_e32 v12, v9
	v_fmac_f32_e32 v11, 0x32a5705f, v8
	v_sub_f32_e32 v9, v9, v12
	v_add_f32_e32 v9, v9, v11
	s_and_b64 s[2:3], s[2:3], s[18:19]
	v_cmp_gt_f32_e64 s[18:19], v7, v6
	v_exp_f32_e32 v9, v9
	v_cvt_i32_f32_e32 v11, v12
	s_and_b64 vcc, s[2:3], s[18:19]
	v_cndmask_b32_e32 v6, v6, v7, vcc
	v_cndmask_b32_e64 v7, v78, v7, s[12:13]
	v_sub_f32_e32 v7, v7, v5
	v_ldexp_f32 v9, v9, v11
	v_mul_f32_e32 v11, 0x3fb8aa3b, v7
	v_fma_f32 v12, v7, s89, -v11
	v_rndne_f32_e32 v13, v11
	v_fmac_f32_e32 v12, 0x32a5705f, v7
	v_sub_f32_e32 v11, v11, v13
	v_add_f32_e32 v11, v11, v12
	v_exp_f32_e32 v11, v11
	v_cvt_i32_f32_e32 v12, v13
	v_cmp_ngt_f32_e64 s[12:13], s84, v8
	v_sub_f32_e32 v5, v6, v5
	v_mul_f32_e32 v6, 0x3fb8aa3b, v5
	v_cndmask_b32_e64 v9, 0, v9, s[12:13]
	v_cmp_nlt_f32_e64 s[12:13], s85, v8
	v_ldexp_f32 v8, v11, v12
	v_rndne_f32_e32 v11, v6
	v_cndmask_b32_e64 v14, v76, v9, s[12:13]
	v_fma_f32 v9, v5, s89, -v6
	v_fmac_f32_e32 v9, 0x32a5705f, v5
	v_sub_f32_e32 v6, v6, v11
	v_add_f32_e32 v6, v6, v9
	v_exp_f32_e32 v6, v6
	v_cvt_i32_f32_e32 v9, v11
	v_cmp_ngt_f32_e64 s[12:13], s84, v7
	v_lshl_add_u32 v12, v4, 2, 0
	v_ldexp_f32 v6, v6, v9
	v_cndmask_b32_e64 v8, 0, v8, s[12:13]
	v_cmp_nlt_f32_e64 s[12:13], s85, v7
	s_nop 1
	v_cndmask_b32_e64 v8, v76, v8, s[12:13]
	v_cmp_ngt_f32_e64 s[12:13], s84, v5
	s_nop 1
	v_cndmask_b32_e64 v6, 0, v6, s[12:13]
	v_cmp_nlt_f32_e64 s[12:13], s85, v5
	v_add_f32_e32 v5, 1.0, v14
	v_add_f32_e32 v5, v5, v8
	v_cndmask_b32_e64 v9, v76, v6, s[12:13]
	v_add_f32_e32 v6, v5, v9
	v_div_scale_f32 v7, s[2:3], v6, v6, 1.0
	v_rcp_f32_e32 v15, v7
	v_cndmask_b32_e64 v5, v10, 29, s[14:15]
	v_cndmask_b32_e64 v5, v5, 30, s[16:17]
	v_cndmask_b32_e64 v5, v5, 31, vcc
	v_fma_f32 v10, -v7, v15, 1.0
	v_fmac_f32_e32 v15, v10, v15
	v_div_scale_f32 v10, vcc, 1.0, v6, 1.0
	v_mul_f32_e32 v16, v10, v15
	v_fma_f32 v11, -v7, v16, v10
	v_fmac_f32_e32 v16, v11, v15
	v_fma_f32 v7, -v7, v16, v10
	v_lshl_add_u32 v10, v2, 2, 0
	ds_add_rtn_u32 v10, v10, v74 offset:42496
	v_lshl_add_u32 v11, v3, 2, 0
	ds_add_rtn_u32 v11, v11, v74 offset:42496
	ds_add_rtn_u32 v12, v12, v74 offset:42496
	v_lshl_add_u32 v13, v5, 2, 0
	ds_add_rtn_u32 v13, v13, v74 offset:42496
	v_div_fmas_f32 v7, v7, v15, v16
	v_div_fixup_f32 v6, v7, v6, 1.0
	v_mul_f32_e32 v7, v14, v6
	v_pk_mul_f32 v[8:9], v[8:9], v[6:7] op_sel_hi:[1,0]
